# GEMM K-loops: the MFMA segments keep s_setprio 1 across both 16-MFMA halves (the s_setprio 0 / s_setprio 1 pair in the middle removed, 36 places)
# speedup vs baseline: 1.1290x; 1.0003x over previous
.LBB0_130:
	s_add_u32 s4, s38, 0x80
	s_addc_u32 s5, s39, 0
	s_add_i32 s31, 0, 0x10000
	s_cmp_eq_u32 s29, 28
	s_cselect_b32 s5, s35, s5
	s_cselect_b32 s4, s34, s4
	v_add_u32_e32 v146, s31, v148
	s_cselect_b32 s43, s37, s15
	s_cselect_b32 s42, s36, s14
	s_add_i32 s68, 0, 0x14000
	ds_read_b128 v[152:155], v146
	ds_read_b128 v[156:159], v146 offset:1024
	ds_read_b128 v[160:163], v146 offset:2048
	ds_read_b128 v[164:167], v146 offset:3072
	v_add_u32_e32 v146, s68, v148
	ds_read_b128 v[168:171], v146
	ds_read_b128 v[172:175], v146 offset:1024
	ds_read_b128 v[176:179], v146 offset:2048
	ds_read_b128 v[180:183], v146 offset:3072
	v_lshl_add_u64 v[146:147], s[38:39], 0, v[144:145]
	s_add_i32 m0, s48, 0xc000
	ds_read_b128 v[184:187], v150
	ds_read_b128 v[188:191], v150 offset:1024
	ds_read_b128 v[192:195], v150 offset:2048
	ds_read_b128 v[196:199], v150 offset:3072
	ds_read_b128 v[224:227], v150 offset:4096
	ds_read_b128 v[228:231], v150 offset:5120
	ds_read_b128 v[238:241], v150 offset:6144
	ds_read_b128 v[242:245], v150 offset:7168
	global_load_lds_dwordx4 v[146:147], off
	v_lshl_add_u64 v[146:147], s[38:39], 0, v[142:143]
	s_add_i32 m0, s48, 0xe000
	s_nop 0
	global_load_lds_dwordx4 v[146:147], off
	s_waitcnt vmcnt(8)
	s_waitcnt lgkmcnt(0)
	s_barrier
	s_setprio 1
	s_waitcnt lgkmcnt(0)
	v_mfma_f32_16x16x32_bf16 v[128:131], v[152:155], v[184:187], v[128:131]
	v_mfma_f32_16x16x32_bf16 v[124:127], v[160:163], v[184:187], v[124:127]
	v_mfma_f32_16x16x32_bf16 v[120:123], v[152:155], v[192:195], v[120:123]
	v_mfma_f32_16x16x32_bf16 v[112:115], v[160:163], v[192:195], v[112:115]
	v_mfma_f32_16x16x32_bf16 v[104:107], v[152:155], v[224:227], v[104:107]
	v_mfma_f32_16x16x32_bf16 v[96:99], v[160:163], v[224:227], v[96:99]
	v_mfma_f32_16x16x32_bf16 v[88:91], v[152:155], v[238:241], v[88:91]
	v_mfma_f32_16x16x32_bf16 v[80:83], v[160:163], v[238:241], v[80:83]
	v_mfma_f32_16x16x32_bf16 v[128:131], v[156:159], v[188:191], v[128:131]
	v_mfma_f32_16x16x32_bf16 v[124:127], v[164:167], v[188:191], v[124:127]
	v_mfma_f32_16x16x32_bf16 v[120:123], v[156:159], v[196:199], v[120:123]
	v_mfma_f32_16x16x32_bf16 v[112:115], v[164:167], v[196:199], v[112:115]
	v_mfma_f32_16x16x32_bf16 v[104:107], v[156:159], v[228:231], v[104:107]
	v_mfma_f32_16x16x32_bf16 v[96:99], v[164:167], v[228:231], v[96:99]
	v_mfma_f32_16x16x32_bf16 v[88:91], v[156:159], v[242:245], v[88:91]
	v_mfma_f32_16x16x32_bf16 v[80:83], v[164:167], v[242:245], v[80:83]
	v_mfma_f32_16x16x32_bf16 v[116:119], v[168:171], v[184:187], v[116:119]
	v_mfma_f32_16x16x32_bf16 v[108:111], v[176:179], v[184:187], v[108:111]
	v_mfma_f32_16x16x32_bf16 v[100:103], v[168:171], v[192:195], v[100:103]
	v_mfma_f32_16x16x32_bf16 v[92:95], v[176:179], v[192:195], v[92:95]
	v_mfma_f32_16x16x32_bf16 v[84:87], v[168:171], v[224:227], v[84:87]
	v_mfma_f32_16x16x32_bf16 v[76:79], v[176:179], v[224:227], v[76:79]
	v_mfma_f32_16x16x32_bf16 v[72:75], v[168:171], v[238:241], v[72:75]
	v_mfma_f32_16x16x32_bf16 v[68:71], v[176:179], v[238:241], v[68:71]
	v_mfma_f32_16x16x32_bf16 v[116:119], v[172:175], v[188:191], v[116:119]
	v_mfma_f32_16x16x32_bf16 v[108:111], v[180:183], v[188:191], v[108:111]
	v_mfma_f32_16x16x32_bf16 v[100:103], v[172:175], v[196:199], v[100:103]
	v_mfma_f32_16x16x32_bf16 v[92:95], v[180:183], v[196:199], v[92:95]
	v_mfma_f32_16x16x32_bf16 v[84:87], v[172:175], v[228:231], v[84:87]
	v_mfma_f32_16x16x32_bf16 v[76:79], v[180:183], v[228:231], v[76:79]
	v_mfma_f32_16x16x32_bf16 v[72:75], v[172:175], v[242:245], v[72:75]
	v_mfma_f32_16x16x32_bf16 v[68:71], v[180:183], v[242:245], v[68:71]
	s_setprio 0
	s_barrier
	s_add_i32 s31, s31, s47
	v_lshl_add_u64 v[146:147], s[42:43], 0, v[34:35]
	s_mov_b32 m0, s31
	ds_read_b128 v[184:187], v150 offset:16384
	ds_read_b128 v[188:191], v150 offset:17408
	ds_read_b128 v[192:195], v150 offset:18432
	ds_read_b128 v[196:199], v150 offset:19456
	ds_read_b128 v[224:227], v150 offset:20480
	ds_read_b128 v[228:231], v150 offset:21504
	ds_read_b128 v[238:241], v150 offset:22528
	ds_read_b128 v[242:245], v150 offset:23552
	global_load_lds_dwordx4 v[146:147], off
	s_add_i32 m0, s31, 0x2000
	s_add_u32 s64, s42, 0x80000
	v_lshl_add_u64 v[212:213], s[42:43], 0, v[132:133]
	s_addc_u32 s65, s43, 0
	s_add_i32 s31, s68, s47
	global_load_lds_dwordx4 v[212:213], off
	v_lshl_add_u64 v[232:233], s[64:65], 0, v[34:35]
	s_mov_b32 m0, s31
	v_lshl_add_u64 v[246:247], s[4:5], 0, v[134:135]
	global_load_lds_dwordx4 v[232:233], off
	v_lshl_add_u64 v[232:233], s[64:65], 0, v[132:133]
	s_add_i32 m0, s31, 0x2000
	s_nop 0
	global_load_lds_dwordx4 v[232:233], off
	v_lshl_add_u64 v[232:233], s[4:5], 0, v[138:139]
	s_mov_b32 m0, s48
	s_nop 0
	global_load_lds_dwordx4 v[232:233], off
	s_mov_b32 m0, s49
	s_nop 0
	global_load_lds_dwordx4 v[246:247], off
	s_waitcnt vmcnt(8)
	s_waitcnt lgkmcnt(0)
	s_barrier
	s_setprio 1
	s_waitcnt lgkmcnt(0)
	v_mfma_f32_16x16x32_bf16 v[64:67], v[152:155], v[184:187], v[64:67]
	v_mfma_f32_16x16x32_bf16 v[60:63], v[160:163], v[184:187], v[60:63]
	v_mfma_f32_16x16x32_bf16 v[52:55], v[152:155], v[192:195], v[52:55]
	v_mfma_f32_16x16x32_bf16 v[44:47], v[160:163], v[192:195], v[44:47]
	v_mfma_f32_16x16x32_bf16 v[36:39], v[152:155], v[224:227], v[36:39]
	v_mfma_f32_16x16x32_bf16 v[26:29], v[160:163], v[224:227], v[26:29]
	v_mfma_f32_16x16x32_bf16 v[18:21], v[152:155], v[238:241], v[18:21]
	v_mfma_f32_16x16x32_bf16 v[10:13], v[160:163], v[238:241], v[10:13]
	v_mfma_f32_16x16x32_bf16 v[64:67], v[156:159], v[188:191], v[64:67]
	v_mfma_f32_16x16x32_bf16 v[60:63], v[164:167], v[188:191], v[60:63]
	v_mfma_f32_16x16x32_bf16 v[52:55], v[156:159], v[196:199], v[52:55]
	v_mfma_f32_16x16x32_bf16 v[44:47], v[164:167], v[196:199], v[44:47]
	v_mfma_f32_16x16x32_bf16 v[36:39], v[156:159], v[228:231], v[36:39]
	v_mfma_f32_16x16x32_bf16 v[26:29], v[164:167], v[228:231], v[26:29]
	v_mfma_f32_16x16x32_bf16 v[18:21], v[156:159], v[242:245], v[18:21]
	v_mfma_f32_16x16x32_bf16 v[10:13], v[164:167], v[242:245], v[10:13]
	v_mfma_f32_16x16x32_bf16 v[56:59], v[168:171], v[184:187], v[56:59]
	v_mfma_f32_16x16x32_bf16 v[48:51], v[176:179], v[184:187], v[48:51]
	v_mfma_f32_16x16x32_bf16 v[40:43], v[168:171], v[192:195], v[40:43]
	v_mfma_f32_16x16x32_bf16 v[30:33], v[176:179], v[192:195], v[30:33]
	v_mfma_f32_16x16x32_bf16 v[22:25], v[168:171], v[224:227], v[22:25]
	v_mfma_f32_16x16x32_bf16 v[14:17], v[176:179], v[224:227], v[14:17]
	v_mfma_f32_16x16x32_bf16 v[6:9], v[168:171], v[238:241], v[6:9]
	v_mfma_f32_16x16x32_bf16 v[2:5], v[176:179], v[238:241], v[2:5]
	v_mfma_f32_16x16x32_bf16 v[56:59], v[172:175], v[188:191], v[56:59]
	v_mfma_f32_16x16x32_bf16 v[48:51], v[180:183], v[188:191], v[48:51]
	v_mfma_f32_16x16x32_bf16 v[40:43], v[172:175], v[196:199], v[40:43]
	v_mfma_f32_16x16x32_bf16 v[30:33], v[180:183], v[196:199], v[30:33]
	v_mfma_f32_16x16x32_bf16 v[22:25], v[172:175], v[228:231], v[22:25]
	v_mfma_f32_16x16x32_bf16 v[14:17], v[180:183], v[228:231], v[14:17]
	v_mfma_f32_16x16x32_bf16 v[6:9], v[172:175], v[242:245], v[6:9]
	v_mfma_f32_16x16x32_bf16 v[2:5], v[180:183], v[242:245], v[2:5]
	s_setprio 0
	s_barrier
	s_add_i32 s31, 0, 0x18000
	v_add_u32_e32 v151, s31, v148
	s_add_i32 s64, 0, 0x1c000
	ds_read_b128 v[152:155], v151
	ds_read_b128 v[156:159], v151 offset:1024
	ds_read_b128 v[160:163], v151 offset:2048
	ds_read_b128 v[164:167], v151 offset:3072
	v_add_u32_e32 v151, s64, v148
	ds_read_b128 v[168:171], v151
	ds_read_b128 v[172:175], v151 offset:1024
	ds_read_b128 v[176:179], v151 offset:2048
	ds_read_b128 v[180:183], v151 offset:3072
	s_mov_b32 m0, s50
	v_lshl_add_u64 v[248:249], s[4:5], 0, v[140:141]
	ds_read_b128 v[184:187], v150 offset:32768
	ds_read_b128 v[188:191], v150 offset:33792
	ds_read_b128 v[192:195], v150 offset:34816
	ds_read_b128 v[196:199], v150 offset:35840
	ds_read_b128 v[224:227], v150 offset:36864
	ds_read_b128 v[228:231], v150 offset:37888
	ds_read_b128 v[238:241], v150 offset:38912
	ds_read_b128 v[242:245], v150 offset:39936
	global_load_lds_dwordx4 v[248:249], off
	v_lshl_add_u64 v[248:249], s[4:5], 0, v[136:137]
	s_mov_b32 m0, s51
	s_nop 0
	global_load_lds_dwordx4 v[248:249], off
	s_waitcnt vmcnt(8)
	s_waitcnt lgkmcnt(0)
	s_barrier
	s_setprio 1
	s_waitcnt lgkmcnt(0)
	v_mfma_f32_16x16x32_bf16 v[128:131], v[152:155], v[184:187], v[128:131]
	v_mfma_f32_16x16x32_bf16 v[124:127], v[160:163], v[184:187], v[124:127]
	v_mfma_f32_16x16x32_bf16 v[120:123], v[152:155], v[192:195], v[120:123]
	v_mfma_f32_16x16x32_bf16 v[112:115], v[160:163], v[192:195], v[112:115]
	v_mfma_f32_16x16x32_bf16 v[104:107], v[152:155], v[224:227], v[104:107]
	v_mfma_f32_16x16x32_bf16 v[96:99], v[160:163], v[224:227], v[96:99]
	v_mfma_f32_16x16x32_bf16 v[88:91], v[152:155], v[238:241], v[88:91]
	v_mfma_f32_16x16x32_bf16 v[80:83], v[160:163], v[238:241], v[80:83]
	v_mfma_f32_16x16x32_bf16 v[128:131], v[156:159], v[188:191], v[128:131]
	v_mfma_f32_16x16x32_bf16 v[124:127], v[164:167], v[188:191], v[124:127]
	v_mfma_f32_16x16x32_bf16 v[120:123], v[156:159], v[196:199], v[120:123]
	v_mfma_f32_16x16x32_bf16 v[112:115], v[164:167], v[196:199], v[112:115]
	v_mfma_f32_16x16x32_bf16 v[104:107], v[156:159], v[228:231], v[104:107]
	v_mfma_f32_16x16x32_bf16 v[96:99], v[164:167], v[228:231], v[96:99]
	v_mfma_f32_16x16x32_bf16 v[88:91], v[156:159], v[242:245], v[88:91]
	v_mfma_f32_16x16x32_bf16 v[80:83], v[164:167], v[242:245], v[80:83]
	v_mfma_f32_16x16x32_bf16 v[116:119], v[168:171], v[184:187], v[116:119]
	v_mfma_f32_16x16x32_bf16 v[108:111], v[176:179], v[184:187], v[108:111]
	v_mfma_f32_16x16x32_bf16 v[100:103], v[168:171], v[192:195], v[100:103]
	v_mfma_f32_16x16x32_bf16 v[92:95], v[176:179], v[192:195], v[92:95]
	v_mfma_f32_16x16x32_bf16 v[84:87], v[168:171], v[224:227], v[84:87]
	v_mfma_f32_16x16x32_bf16 v[76:79], v[176:179], v[224:227], v[76:79]
	v_mfma_f32_16x16x32_bf16 v[72:75], v[168:171], v[238:241], v[72:75]
	v_mfma_f32_16x16x32_bf16 v[68:71], v[176:179], v[238:241], v[68:71]
	v_mfma_f32_16x16x32_bf16 v[116:119], v[172:175], v[188:191], v[116:119]
	v_mfma_f32_16x16x32_bf16 v[108:111], v[180:183], v[188:191], v[108:111]
	v_mfma_f32_16x16x32_bf16 v[100:103], v[172:175], v[196:199], v[100:103]
	v_mfma_f32_16x16x32_bf16 v[92:95], v[180:183], v[196:199], v[92:95]
	v_mfma_f32_16x16x32_bf16 v[84:87], v[172:175], v[228:231], v[84:87]
	v_mfma_f32_16x16x32_bf16 v[76:79], v[180:183], v[228:231], v[76:79]
	v_mfma_f32_16x16x32_bf16 v[72:75], v[172:175], v[242:245], v[72:75]
	v_mfma_f32_16x16x32_bf16 v[68:71], v[180:183], v[242:245], v[68:71]
	s_setprio 0
	s_barrier
	s_add_i32 s4, s31, s47
	v_lshl_add_u64 v[146:147], v[146:147], 0, s[78:79]
	s_mov_b32 m0, s4
	ds_read_b128 v[184:187], v150 offset:49152
	ds_read_b128 v[188:191], v150 offset:50176
	ds_read_b128 v[192:195], v150 offset:51200
	ds_read_b128 v[196:199], v150 offset:52224
	ds_read_b128 v[224:227], v150 offset:53248
	ds_read_b128 v[228:231], v150 offset:54272
	ds_read_b128 v[238:241], v150 offset:55296
	ds_read_b128 v[242:245], v150 offset:56320
	global_load_lds_dwordx4 v[146:147], off
	s_add_i32 m0, s4, 0x2000
	s_add_u32 s4, s42, 0x80080
	v_lshl_add_u64 v[146:147], v[212:213], 0, s[78:79]
	s_addc_u32 s5, s43, 0
	s_add_i32 s31, s64, s47
	global_load_lds_dwordx4 v[146:147], off
	v_lshl_add_u64 v[146:147], s[4:5], 0, v[34:35]
	s_mov_b32 m0, s31
	s_nop 0
	global_load_lds_dwordx4 v[146:147], off
	v_lshl_add_u64 v[146:147], s[4:5], 0, v[132:133]
	s_add_i32 m0, s31, 0x2000
	s_nop 0
	global_load_lds_dwordx4 v[146:147], off
	v_lshl_add_u64 v[146:147], v[232:233], 0, s[78:79]
	s_mov_b32 m0, s52
	s_nop 0
	global_load_lds_dwordx4 v[146:147], off
	v_lshl_add_u64 v[146:147], v[246:247], 0, s[78:79]
	s_mov_b32 m0, s53
	s_nop 0
	global_load_lds_dwordx4 v[146:147], off
	s_waitcnt vmcnt(8)
	s_waitcnt lgkmcnt(0)
	s_barrier
	s_setprio 1
	s_waitcnt lgkmcnt(0)
	v_mfma_f32_16x16x32_bf16 v[64:67], v[152:155], v[184:187], v[64:67]
	v_mfma_f32_16x16x32_bf16 v[60:63], v[160:163], v[184:187], v[60:63]
	v_mfma_f32_16x16x32_bf16 v[52:55], v[152:155], v[192:195], v[52:55]
	v_mfma_f32_16x16x32_bf16 v[44:47], v[160:163], v[192:195], v[44:47]
	v_mfma_f32_16x16x32_bf16 v[36:39], v[152:155], v[224:227], v[36:39]
	v_mfma_f32_16x16x32_bf16 v[26:29], v[160:163], v[224:227], v[26:29]
	v_mfma_f32_16x16x32_bf16 v[18:21], v[152:155], v[238:241], v[18:21]
	v_mfma_f32_16x16x32_bf16 v[10:13], v[160:163], v[238:241], v[10:13]
	v_mfma_f32_16x16x32_bf16 v[64:67], v[156:159], v[188:191], v[64:67]
	v_mfma_f32_16x16x32_bf16 v[60:63], v[164:167], v[188:191], v[60:63]
	v_mfma_f32_16x16x32_bf16 v[52:55], v[156:159], v[196:199], v[52:55]
	v_mfma_f32_16x16x32_bf16 v[44:47], v[164:167], v[196:199], v[44:47]
	v_mfma_f32_16x16x32_bf16 v[36:39], v[156:159], v[228:231], v[36:39]
	v_mfma_f32_16x16x32_bf16 v[26:29], v[164:167], v[228:231], v[26:29]
	v_mfma_f32_16x16x32_bf16 v[18:21], v[156:159], v[242:245], v[18:21]
	v_mfma_f32_16x16x32_bf16 v[10:13], v[164:167], v[242:245], v[10:13]
	v_mfma_f32_16x16x32_bf16 v[56:59], v[168:171], v[184:187], v[56:59]
	v_mfma_f32_16x16x32_bf16 v[48:51], v[176:179], v[184:187], v[48:51]
	v_mfma_f32_16x16x32_bf16 v[40:43], v[168:171], v[192:195], v[40:43]
	v_mfma_f32_16x16x32_bf16 v[30:33], v[176:179], v[192:195], v[30:33]
	v_mfma_f32_16x16x32_bf16 v[22:25], v[168:171], v[224:227], v[22:25]
	v_mfma_f32_16x16x32_bf16 v[14:17], v[176:179], v[224:227], v[14:17]
	v_mfma_f32_16x16x32_bf16 v[6:9], v[168:171], v[238:241], v[6:9]
	v_mfma_f32_16x16x32_bf16 v[2:5], v[176:179], v[238:241], v[2:5]
	v_mfma_f32_16x16x32_bf16 v[56:59], v[172:175], v[188:191], v[56:59]
	v_mfma_f32_16x16x32_bf16 v[48:51], v[180:183], v[188:191], v[48:51]
	v_mfma_f32_16x16x32_bf16 v[40:43], v[172:175], v[196:199], v[40:43]
	v_mfma_f32_16x16x32_bf16 v[30:33], v[180:183], v[196:199], v[30:33]
	v_mfma_f32_16x16x32_bf16 v[22:25], v[172:175], v[228:231], v[22:25]
	v_mfma_f32_16x16x32_bf16 v[14:17], v[180:183], v[228:231], v[14:17]
	v_mfma_f32_16x16x32_bf16 v[6:9], v[172:175], v[242:245], v[6:9]
	v_mfma_f32_16x16x32_bf16 v[2:5], v[180:183], v[242:245], v[2:5]
	s_setprio 0
	s_barrier
	s_add_i32 s29, s29, 2
	s_add_u32 s14, s14, 0x100
	s_addc_u32 s15, s15, 0
	s_add_u32 s38, s38, 0x100
	s_addc_u32 s39, s39, 0
	s_cmp_gt_u32 s29, 29
	s_cbranch_scc0 .LBB0_130
	s_and_b64 vcc, exec, s[22:23]
	s_cbranch_vccz .LBB0_133
	s_barrier

.LBB0_322:
	s_add_u32 s4, s38, s48
	s_addc_u32 s5, s39, s49
	s_add_u32 s29, s4, 0x100
	s_addc_u32 s31, s5, 0
	s_and_b64 s[14:15], s[46:47], exec
	s_cselect_b32 s50, s34, s29
	s_cselect_b32 s51, s35, s31
	s_add_u32 s14, s42, s48
	s_addc_u32 s15, s43, s49
	s_add_u32 s29, s14, 0x100
	s_addc_u32 s31, s15, 0
	s_add_i32 s84, 0, 0x10000
	s_and_b64 s[14:15], s[46:47], exec
	s_cselect_b32 s49, s37, s31
	s_cselect_b32 s48, s36, s29
	s_add_i32 s47, 0, 0x14000
	v_add_u32_e32 v144, s84, v146
	s_add_i32 vcc_lo, s84, s57
	ds_read_b128 v[148:151], v144
	ds_read_b128 v[152:155], v144 offset:1024
	ds_read_b128 v[156:159], v144 offset:2048
	ds_read_b128 v[160:163], v144 offset:3072
	v_add_u32_e32 v144, s47, v146
	s_add_i32 m0, s64, 0xc000
	s_add_i32 s85, s64, 0xe000
	s_add_i32 s89, vcc_lo, 0x2000
	ds_read_b128 v[164:167], v144
	ds_read_b128 v[168:171], v144 offset:1024
	ds_read_b128 v[172:175], v144 offset:2048
	ds_read_b128 v[176:179], v144 offset:3072
	s_add_u32 s52, s48, 0x10000
	s_addc_u32 s53, s49, 0
	s_add_i32 s31, 0, 0x18000
	s_add_i32 s96, s47, s57
	s_add_i32 s15, s31, s57
	s_add_i32 s93, s96, 0x2000
	s_add_i32 s29, 0, 0x1c000
	s_add_i32 s14, s15, 0x2000
	s_add_u32 s46, s48, 0x10080
	s_addc_u32 s47, s49, 0
	s_add_i32 vcc_hi, s29, s57
	s_add_i32 s84, vcc_hi, 0x2000
	v_lshl_add_u64 v[144:145], s[4:5], 0, v[140:141]
	v_lshl_add_u64 v[144:145], v[144:145], 0, s[78:79]
	ds_read_b128 v[180:183], v147
	ds_read_b128 v[184:187], v147 offset:1024
	ds_read_b128 v[188:191], v147 offset:2048
	ds_read_b128 v[192:195], v147 offset:3072
	ds_read_b128 v[196:199], v147 offset:4096
	ds_read_b128 v[224:227], v147 offset:5120
	ds_read_b128 v[228:231], v147 offset:6144
	ds_read_b128 v[238:241], v147 offset:7168
	global_load_lds_dwordx4 v[144:145], off
	v_lshl_add_u64 v[144:145], s[4:5], 0, v[136:137]
	v_lshl_add_u64 v[144:145], v[144:145], 0, s[78:79]
	s_mov_b32 m0, s85
	s_nop 0
	global_load_lds_dwordx4 v[144:145], off
	s_waitcnt vmcnt(8)
	s_waitcnt lgkmcnt(0)
	s_barrier
	s_setprio 1
	s_waitcnt lgkmcnt(0)
	v_mfma_f32_16x16x32_bf16 v[128:131], v[148:151], v[180:183], v[128:131]
	v_mfma_f32_16x16x32_bf16 v[124:127], v[156:159], v[180:183], v[124:127]
	v_mfma_f32_16x16x32_bf16 v[120:123], v[148:151], v[188:191], v[120:123]
	v_mfma_f32_16x16x32_bf16 v[116:119], v[156:159], v[188:191], v[116:119]
	v_mfma_f32_16x16x32_bf16 v[104:107], v[148:151], v[196:199], v[104:107]
	v_mfma_f32_16x16x32_bf16 v[100:103], v[156:159], v[196:199], v[100:103]
	v_mfma_f32_16x16x32_bf16 v[88:91], v[148:151], v[228:231], v[88:91]
	v_mfma_f32_16x16x32_bf16 v[84:87], v[156:159], v[228:231], v[84:87]
	v_mfma_f32_16x16x32_bf16 v[128:131], v[152:155], v[184:187], v[128:131]
	v_mfma_f32_16x16x32_bf16 v[124:127], v[160:163], v[184:187], v[124:127]
	v_mfma_f32_16x16x32_bf16 v[120:123], v[152:155], v[192:195], v[120:123]
	v_mfma_f32_16x16x32_bf16 v[116:119], v[160:163], v[192:195], v[116:119]
	v_mfma_f32_16x16x32_bf16 v[104:107], v[152:155], v[224:227], v[104:107]
	v_mfma_f32_16x16x32_bf16 v[100:103], v[160:163], v[224:227], v[100:103]
	v_mfma_f32_16x16x32_bf16 v[88:91], v[152:155], v[238:241], v[88:91]
	v_mfma_f32_16x16x32_bf16 v[84:87], v[160:163], v[238:241], v[84:87]
	v_mfma_f32_16x16x32_bf16 v[112:115], v[164:167], v[180:183], v[112:115]
	v_mfma_f32_16x16x32_bf16 v[108:111], v[172:175], v[180:183], v[108:111]
	v_mfma_f32_16x16x32_bf16 v[96:99], v[164:167], v[188:191], v[96:99]
	v_mfma_f32_16x16x32_bf16 v[92:95], v[172:175], v[188:191], v[92:95]
	v_mfma_f32_16x16x32_bf16 v[80:83], v[164:167], v[196:199], v[80:83]
	v_mfma_f32_16x16x32_bf16 v[76:79], v[172:175], v[196:199], v[76:79]
	v_mfma_f32_16x16x32_bf16 v[72:75], v[164:167], v[228:231], v[72:75]
	v_mfma_f32_16x16x32_bf16 v[68:71], v[172:175], v[228:231], v[68:71]
	v_mfma_f32_16x16x32_bf16 v[112:115], v[168:171], v[184:187], v[112:115]
	v_mfma_f32_16x16x32_bf16 v[108:111], v[176:179], v[184:187], v[108:111]
	v_mfma_f32_16x16x32_bf16 v[96:99], v[168:171], v[192:195], v[96:99]
	v_mfma_f32_16x16x32_bf16 v[92:95], v[176:179], v[192:195], v[92:95]
	v_mfma_f32_16x16x32_bf16 v[80:83], v[168:171], v[224:227], v[80:83]
	v_mfma_f32_16x16x32_bf16 v[76:79], v[176:179], v[224:227], v[76:79]
	v_mfma_f32_16x16x32_bf16 v[72:75], v[168:171], v[238:241], v[72:75]
	v_mfma_f32_16x16x32_bf16 v[68:71], v[176:179], v[238:241], v[68:71]
	s_setprio 0
	s_barrier
	s_mov_b32 m0, vcc_lo
	v_lshl_add_u64 v[144:145], s[48:49], 0, v[34:35]
	ds_read_b128 v[180:183], v147 offset:16384
	ds_read_b128 v[184:187], v147 offset:17408
	ds_read_b128 v[188:191], v147 offset:18432
	ds_read_b128 v[192:195], v147 offset:19456
	ds_read_b128 v[196:199], v147 offset:20480
	ds_read_b128 v[224:227], v147 offset:21504
	ds_read_b128 v[228:231], v147 offset:22528
	ds_read_b128 v[238:241], v147 offset:23552
	global_load_lds_dwordx4 v[144:145], off
	v_lshl_add_u64 v[212:213], s[48:49], 0, v[132:133]
	s_mov_b32 m0, s89
	v_lshl_add_u64 v[232:233], s[52:53], 0, v[34:35]
	global_load_lds_dwordx4 v[212:213], off
	s_mov_b32 m0, s96
	v_lshl_add_u64 v[242:243], s[50:51], 0, v[134:135]
	global_load_lds_dwordx4 v[232:233], off
	v_lshl_add_u64 v[232:233], s[52:53], 0, v[132:133]
	s_mov_b32 m0, s93
	s_nop 0
	global_load_lds_dwordx4 v[232:233], off
	v_lshl_add_u64 v[232:233], s[50:51], 0, v[138:139]
	s_mov_b32 m0, s64
	s_nop 0
	global_load_lds_dwordx4 v[232:233], off
	s_mov_b32 m0, s65
	s_nop 0
	global_load_lds_dwordx4 v[242:243], off
	s_waitcnt vmcnt(8)
	s_waitcnt lgkmcnt(0)
	s_barrier
	s_setprio 1
	s_waitcnt lgkmcnt(0)
	v_mfma_f32_16x16x32_bf16 v[64:67], v[148:151], v[180:183], v[64:67]
	v_mfma_f32_16x16x32_bf16 v[60:63], v[156:159], v[180:183], v[60:63]
	v_mfma_f32_16x16x32_bf16 v[56:59], v[148:151], v[188:191], v[56:59]
	v_mfma_f32_16x16x32_bf16 v[52:55], v[156:159], v[188:191], v[52:55]
	v_mfma_f32_16x16x32_bf16 v[40:43], v[148:151], v[196:199], v[40:43]
	v_mfma_f32_16x16x32_bf16 v[36:39], v[156:159], v[196:199], v[36:39]
	v_mfma_f32_16x16x32_bf16 v[22:25], v[148:151], v[228:231], v[22:25]
	v_mfma_f32_16x16x32_bf16 v[18:21], v[156:159], v[228:231], v[18:21]
	v_mfma_f32_16x16x32_bf16 v[64:67], v[152:155], v[184:187], v[64:67]
	v_mfma_f32_16x16x32_bf16 v[60:63], v[160:163], v[184:187], v[60:63]
	v_mfma_f32_16x16x32_bf16 v[56:59], v[152:155], v[192:195], v[56:59]
	v_mfma_f32_16x16x32_bf16 v[52:55], v[160:163], v[192:195], v[52:55]
	v_mfma_f32_16x16x32_bf16 v[40:43], v[152:155], v[224:227], v[40:43]
	v_mfma_f32_16x16x32_bf16 v[36:39], v[160:163], v[224:227], v[36:39]
	v_mfma_f32_16x16x32_bf16 v[22:25], v[152:155], v[238:241], v[22:25]
	v_mfma_f32_16x16x32_bf16 v[18:21], v[160:163], v[238:241], v[18:21]
	v_mfma_f32_16x16x32_bf16 v[48:51], v[164:167], v[180:183], v[48:51]
	v_mfma_f32_16x16x32_bf16 v[44:47], v[172:175], v[180:183], v[44:47]
	v_mfma_f32_16x16x32_bf16 v[30:33], v[164:167], v[188:191], v[30:33]
	v_mfma_f32_16x16x32_bf16 v[26:29], v[172:175], v[188:191], v[26:29]
	v_mfma_f32_16x16x32_bf16 v[14:17], v[164:167], v[196:199], v[14:17]
	v_mfma_f32_16x16x32_bf16 v[10:13], v[172:175], v[196:199], v[10:13]
	v_mfma_f32_16x16x32_bf16 v[6:9], v[164:167], v[228:231], v[6:9]
	v_mfma_f32_16x16x32_bf16 v[2:5], v[172:175], v[228:231], v[2:5]
	v_mfma_f32_16x16x32_bf16 v[48:51], v[168:171], v[184:187], v[48:51]
	v_mfma_f32_16x16x32_bf16 v[44:47], v[176:179], v[184:187], v[44:47]
	v_mfma_f32_16x16x32_bf16 v[30:33], v[168:171], v[192:195], v[30:33]
	v_mfma_f32_16x16x32_bf16 v[26:29], v[176:179], v[192:195], v[26:29]
	v_mfma_f32_16x16x32_bf16 v[14:17], v[168:171], v[224:227], v[14:17]
	v_mfma_f32_16x16x32_bf16 v[10:13], v[176:179], v[224:227], v[10:13]
	v_mfma_f32_16x16x32_bf16 v[6:9], v[168:171], v[238:241], v[6:9]
	v_mfma_f32_16x16x32_bf16 v[2:5], v[176:179], v[238:241], v[2:5]
	s_setprio 0
	s_barrier
	v_add_u32_e32 v160, s31, v146
	v_add_u32_e32 v176, s29, v146
	ds_read_b128 v[148:151], v160
	ds_read_b128 v[152:155], v160 offset:1024
	ds_read_b128 v[156:159], v160 offset:2048
	ds_read_b128 v[160:163], v160 offset:3072
	ds_read_b128 v[164:167], v176
	ds_read_b128 v[168:171], v176 offset:1024
	ds_read_b128 v[172:175], v176 offset:2048
	ds_read_b128 v[176:179], v176 offset:3072
	s_mov_b32 m0, s68
	v_lshl_add_u64 v[244:245], s[50:51], 0, v[140:141]
	ds_read_b128 v[180:183], v147 offset:32768
	ds_read_b128 v[184:187], v147 offset:33792
	ds_read_b128 v[188:191], v147 offset:34816
	ds_read_b128 v[192:195], v147 offset:35840
	ds_read_b128 v[196:199], v147 offset:36864
	ds_read_b128 v[224:227], v147 offset:37888
	ds_read_b128 v[228:231], v147 offset:38912
	ds_read_b128 v[238:241], v147 offset:39936
	global_load_lds_dwordx4 v[244:245], off
	v_lshl_add_u64 v[244:245], s[50:51], 0, v[136:137]
	s_mov_b32 m0, s69
	s_nop 0
	global_load_lds_dwordx4 v[244:245], off
	s_waitcnt vmcnt(8)
	s_waitcnt lgkmcnt(0)
	s_barrier
	s_setprio 1
	s_waitcnt lgkmcnt(0)
	v_mfma_f32_16x16x32_bf16 v[128:131], v[148:151], v[180:183], v[128:131]
	v_mfma_f32_16x16x32_bf16 v[124:127], v[156:159], v[180:183], v[124:127]
	v_mfma_f32_16x16x32_bf16 v[120:123], v[148:151], v[188:191], v[120:123]
	v_mfma_f32_16x16x32_bf16 v[116:119], v[156:159], v[188:191], v[116:119]
	v_mfma_f32_16x16x32_bf16 v[104:107], v[148:151], v[196:199], v[104:107]
	v_mfma_f32_16x16x32_bf16 v[100:103], v[156:159], v[196:199], v[100:103]
	v_mfma_f32_16x16x32_bf16 v[88:91], v[148:151], v[228:231], v[88:91]
	v_mfma_f32_16x16x32_bf16 v[84:87], v[156:159], v[228:231], v[84:87]
	v_mfma_f32_16x16x32_bf16 v[128:131], v[152:155], v[184:187], v[128:131]
	v_mfma_f32_16x16x32_bf16 v[124:127], v[160:163], v[184:187], v[124:127]
	v_mfma_f32_16x16x32_bf16 v[120:123], v[152:155], v[192:195], v[120:123]
	v_mfma_f32_16x16x32_bf16 v[116:119], v[160:163], v[192:195], v[116:119]
	v_mfma_f32_16x16x32_bf16 v[104:107], v[152:155], v[224:227], v[104:107]
	v_mfma_f32_16x16x32_bf16 v[100:103], v[160:163], v[224:227], v[100:103]
	v_mfma_f32_16x16x32_bf16 v[88:91], v[152:155], v[238:241], v[88:91]
	v_mfma_f32_16x16x32_bf16 v[84:87], v[160:163], v[238:241], v[84:87]
	v_mfma_f32_16x16x32_bf16 v[112:115], v[164:167], v[180:183], v[112:115]
	v_mfma_f32_16x16x32_bf16 v[108:111], v[172:175], v[180:183], v[108:111]
	v_mfma_f32_16x16x32_bf16 v[96:99], v[164:167], v[188:191], v[96:99]
	v_mfma_f32_16x16x32_bf16 v[92:95], v[172:175], v[188:191], v[92:95]
	v_mfma_f32_16x16x32_bf16 v[80:83], v[164:167], v[196:199], v[80:83]
	v_mfma_f32_16x16x32_bf16 v[76:79], v[172:175], v[196:199], v[76:79]
	v_mfma_f32_16x16x32_bf16 v[72:75], v[164:167], v[228:231], v[72:75]
	v_mfma_f32_16x16x32_bf16 v[68:71], v[172:175], v[228:231], v[68:71]
	v_mfma_f32_16x16x32_bf16 v[112:115], v[168:171], v[184:187], v[112:115]
	v_mfma_f32_16x16x32_bf16 v[108:111], v[176:179], v[184:187], v[108:111]
	v_mfma_f32_16x16x32_bf16 v[96:99], v[168:171], v[192:195], v[96:99]
	v_mfma_f32_16x16x32_bf16 v[92:95], v[176:179], v[192:195], v[92:95]
	v_mfma_f32_16x16x32_bf16 v[80:83], v[168:171], v[224:227], v[80:83]
	v_mfma_f32_16x16x32_bf16 v[76:79], v[176:179], v[224:227], v[76:79]
	v_mfma_f32_16x16x32_bf16 v[72:75], v[168:171], v[238:241], v[72:75]
	v_mfma_f32_16x16x32_bf16 v[68:71], v[176:179], v[238:241], v[68:71]
	s_setprio 0
	s_barrier
	s_mov_b32 m0, s15
	v_lshl_add_u64 v[144:145], v[144:145], 0, s[78:79]
	ds_read_b128 v[180:183], v147 offset:49152
	ds_read_b128 v[184:187], v147 offset:50176
	ds_read_b128 v[188:191], v147 offset:51200
	ds_read_b128 v[192:195], v147 offset:52224
	ds_read_b128 v[196:199], v147 offset:53248
	ds_read_b128 v[224:227], v147 offset:54272
	ds_read_b128 v[228:231], v147 offset:55296
	ds_read_b128 v[238:241], v147 offset:56320
	global_load_lds_dwordx4 v[144:145], off
	v_lshl_add_u64 v[144:145], v[212:213], 0, s[78:79]
	s_mov_b32 m0, s14
	s_nop 0
	global_load_lds_dwordx4 v[144:145], off
	v_lshl_add_u64 v[144:145], s[46:47], 0, v[34:35]
	s_mov_b32 m0, vcc_hi
	s_nop 0
	global_load_lds_dwordx4 v[144:145], off
	v_lshl_add_u64 v[144:145], s[46:47], 0, v[132:133]
	s_mov_b32 m0, s84
	s_nop 0
	global_load_lds_dwordx4 v[144:145], off
	v_lshl_add_u64 v[144:145], v[232:233], 0, s[78:79]
	s_mov_b32 m0, s71
	s_nop 0
	global_load_lds_dwordx4 v[144:145], off
	v_lshl_add_u64 v[144:145], v[242:243], 0, s[78:79]
	s_mov_b32 m0, s74
	s_nop 0
	global_load_lds_dwordx4 v[144:145], off
	s_waitcnt vmcnt(8)
	s_waitcnt lgkmcnt(0)
	s_barrier
	s_setprio 1
	s_waitcnt lgkmcnt(0)
	v_mfma_f32_16x16x32_bf16 v[64:67], v[148:151], v[180:183], v[64:67]
	v_mfma_f32_16x16x32_bf16 v[60:63], v[156:159], v[180:183], v[60:63]
	v_mfma_f32_16x16x32_bf16 v[56:59], v[148:151], v[188:191], v[56:59]
	v_mfma_f32_16x16x32_bf16 v[52:55], v[156:159], v[188:191], v[52:55]
	v_mfma_f32_16x16x32_bf16 v[40:43], v[148:151], v[196:199], v[40:43]
	v_mfma_f32_16x16x32_bf16 v[36:39], v[156:159], v[196:199], v[36:39]
	v_mfma_f32_16x16x32_bf16 v[22:25], v[148:151], v[228:231], v[22:25]
	v_mfma_f32_16x16x32_bf16 v[18:21], v[156:159], v[228:231], v[18:21]
	v_mfma_f32_16x16x32_bf16 v[64:67], v[152:155], v[184:187], v[64:67]
	v_mfma_f32_16x16x32_bf16 v[60:63], v[160:163], v[184:187], v[60:63]
	v_mfma_f32_16x16x32_bf16 v[56:59], v[152:155], v[192:195], v[56:59]
	v_mfma_f32_16x16x32_bf16 v[52:55], v[160:163], v[192:195], v[52:55]
	v_mfma_f32_16x16x32_bf16 v[40:43], v[152:155], v[224:227], v[40:43]
	v_mfma_f32_16x16x32_bf16 v[36:39], v[160:163], v[224:227], v[36:39]
	v_mfma_f32_16x16x32_bf16 v[22:25], v[152:155], v[238:241], v[22:25]
	v_mfma_f32_16x16x32_bf16 v[18:21], v[160:163], v[238:241], v[18:21]
	v_mfma_f32_16x16x32_bf16 v[48:51], v[164:167], v[180:183], v[48:51]
	v_mfma_f32_16x16x32_bf16 v[44:47], v[172:175], v[180:183], v[44:47]
	v_mfma_f32_16x16x32_bf16 v[30:33], v[164:167], v[188:191], v[30:33]
	v_mfma_f32_16x16x32_bf16 v[26:29], v[172:175], v[188:191], v[26:29]
	v_mfma_f32_16x16x32_bf16 v[14:17], v[164:167], v[196:199], v[14:17]
	v_mfma_f32_16x16x32_bf16 v[10:13], v[172:175], v[196:199], v[10:13]
	v_mfma_f32_16x16x32_bf16 v[6:9], v[164:167], v[228:231], v[6:9]
	v_mfma_f32_16x16x32_bf16 v[2:5], v[172:175], v[228:231], v[2:5]
	v_mfma_f32_16x16x32_bf16 v[48:51], v[168:171], v[184:187], v[48:51]
	v_mfma_f32_16x16x32_bf16 v[44:47], v[176:179], v[184:187], v[44:47]
	v_mfma_f32_16x16x32_bf16 v[30:33], v[168:171], v[192:195], v[30:33]
	v_mfma_f32_16x16x32_bf16 v[26:29], v[176:179], v[192:195], v[26:29]
	v_mfma_f32_16x16x32_bf16 v[14:17], v[168:171], v[224:227], v[14:17]
	v_mfma_f32_16x16x32_bf16 v[10:13], v[176:179], v[224:227], v[10:13]
	v_mfma_f32_16x16x32_bf16 v[6:9], v[168:171], v[238:241], v[6:9]
	v_mfma_f32_16x16x32_bf16 v[2:5], v[176:179], v[238:241], v[2:5]
	s_setprio 0
	s_barrier
	s_andn2_b64 vcc, exec, s[44:45]
	s_mov_b64 s[46:47], -1
	s_mov_b64 s[44:45], 0
	s_mov_b64 s[48:49], 0x100
	s_cbranch_vccz .LBB0_322
	s_and_b64 vcc, exec, s[22:23]
	s_cbranch_vccz .LBB0_325
	s_barrier

.LBB0_349:
	s_add_u32 s4, s36, s44
	s_addc_u32 s5, s37, s45
	s_add_u32 s25, s4, 0x100
	s_addc_u32 s27, s5, 0
	s_and_b64 s[46:47], s[42:43], exec
	s_cselect_b32 s46, s28, s25
	s_cselect_b32 s47, s29, s27
	s_add_u32 s25, s34, s44
	s_addc_u32 s27, s35, s45
	s_add_u32 s25, s25, 0x100
	s_addc_u32 s27, s27, 0
	s_add_i32 s82, 0, 0x10000
	s_and_b64 s[42:43], s[42:43], exec
	s_cselect_b32 s45, s31, s27
	s_cselect_b32 s44, s30, s25
	s_add_i32 s43, 0, 0x14000
	v_add_u32_e32 v142, s82, v144
	s_add_i32 s81, s82, s51
	ds_read_b128 v[148:151], v142
	ds_read_b128 v[152:155], v142 offset:1024
	ds_read_b128 v[156:159], v142 offset:2048
	ds_read_b128 v[160:163], v142 offset:3072
	v_add_u32_e32 v142, s43, v144
	s_add_i32 m0, s52, 0xc000
	s_add_i32 s84, s52, 0xe000
	s_add_i32 s74, s81, 0x2000
	ds_read_b128 v[164:167], v142
	ds_read_b128 v[168:171], v142 offset:1024
	ds_read_b128 v[172:175], v142 offset:2048
	ds_read_b128 v[176:179], v142 offset:3072
	s_add_u32 s48, s44, 0x10000
	s_addc_u32 s49, s45, 0
	s_add_i32 s71, 0, 0x18000
	s_add_i32 s80, s43, s51
	s_add_i32 s27, s71, s51
	s_add_i32 s75, s80, 0x2000
	s_add_i32 s70, 0, 0x1c000
	s_add_i32 s25, s27, 0x2000
	s_add_u32 s42, s44, 0x10080
	s_addc_u32 s43, s45, 0
	s_add_i32 s83, s70, s51
	s_add_i32 s82, s83, 0x2000
	v_lshl_add_u64 v[142:143], s[4:5], 0, v[140:141]
	v_lshl_add_u64 v[142:143], v[142:143], 0, s[78:79]
	ds_read_b128 v[180:183], v146
	ds_read_b128 v[184:187], v146 offset:1024
	ds_read_b128 v[188:191], v146 offset:2048
	ds_read_b128 v[192:195], v146 offset:3072
	ds_read_b128 v[196:199], v146 offset:4096
	ds_read_b128 v[224:227], v146 offset:5120
	ds_read_b128 v[228:231], v146 offset:6144
	ds_read_b128 v[238:241], v146 offset:7168
	global_load_lds_dwordx4 v[142:143], off
	v_lshl_add_u64 v[142:143], s[4:5], 0, v[136:137]
	v_lshl_add_u64 v[142:143], v[142:143], 0, s[78:79]
	s_mov_b32 m0, s84
	s_nop 0
	global_load_lds_dwordx4 v[142:143], off
	s_waitcnt vmcnt(8)
	s_waitcnt lgkmcnt(0)
	s_barrier
	s_setprio 1
	s_waitcnt lgkmcnt(0)
	v_mfma_f32_16x16x32_bf16 v[128:131], v[148:151], v[180:183], v[128:131]
	v_mfma_f32_16x16x32_bf16 v[124:127], v[156:159], v[180:183], v[124:127]
	v_mfma_f32_16x16x32_bf16 v[120:123], v[148:151], v[188:191], v[120:123]
	v_mfma_f32_16x16x32_bf16 v[112:115], v[156:159], v[188:191], v[112:115]
	v_mfma_f32_16x16x32_bf16 v[104:107], v[148:151], v[196:199], v[104:107]
	v_mfma_f32_16x16x32_bf16 v[96:99], v[156:159], v[196:199], v[96:99]
	v_mfma_f32_16x16x32_bf16 v[88:91], v[148:151], v[228:231], v[88:91]
	v_mfma_f32_16x16x32_bf16 v[80:83], v[156:159], v[228:231], v[80:83]
	v_mfma_f32_16x16x32_bf16 v[128:131], v[152:155], v[184:187], v[128:131]
	v_mfma_f32_16x16x32_bf16 v[124:127], v[160:163], v[184:187], v[124:127]
	v_mfma_f32_16x16x32_bf16 v[120:123], v[152:155], v[192:195], v[120:123]
	v_mfma_f32_16x16x32_bf16 v[112:115], v[160:163], v[192:195], v[112:115]
	v_mfma_f32_16x16x32_bf16 v[104:107], v[152:155], v[224:227], v[104:107]
	v_mfma_f32_16x16x32_bf16 v[96:99], v[160:163], v[224:227], v[96:99]
	v_mfma_f32_16x16x32_bf16 v[88:91], v[152:155], v[238:241], v[88:91]
	v_mfma_f32_16x16x32_bf16 v[80:83], v[160:163], v[238:241], v[80:83]
	v_mfma_f32_16x16x32_bf16 v[116:119], v[164:167], v[180:183], v[116:119]
	v_mfma_f32_16x16x32_bf16 v[108:111], v[172:175], v[180:183], v[108:111]
	v_mfma_f32_16x16x32_bf16 v[100:103], v[164:167], v[188:191], v[100:103]
	v_mfma_f32_16x16x32_bf16 v[92:95], v[172:175], v[188:191], v[92:95]
	v_mfma_f32_16x16x32_bf16 v[84:87], v[164:167], v[196:199], v[84:87]
	v_mfma_f32_16x16x32_bf16 v[76:79], v[172:175], v[196:199], v[76:79]
	v_mfma_f32_16x16x32_bf16 v[72:75], v[164:167], v[228:231], v[72:75]
	v_mfma_f32_16x16x32_bf16 v[68:71], v[172:175], v[228:231], v[68:71]
	v_mfma_f32_16x16x32_bf16 v[116:119], v[168:171], v[184:187], v[116:119]
	v_mfma_f32_16x16x32_bf16 v[108:111], v[176:179], v[184:187], v[108:111]
	v_mfma_f32_16x16x32_bf16 v[100:103], v[168:171], v[192:195], v[100:103]
	v_mfma_f32_16x16x32_bf16 v[92:95], v[176:179], v[192:195], v[92:95]
	v_mfma_f32_16x16x32_bf16 v[84:87], v[168:171], v[224:227], v[84:87]
	v_mfma_f32_16x16x32_bf16 v[76:79], v[176:179], v[224:227], v[76:79]
	v_mfma_f32_16x16x32_bf16 v[72:75], v[168:171], v[238:241], v[72:75]
	v_mfma_f32_16x16x32_bf16 v[68:71], v[176:179], v[238:241], v[68:71]
	s_setprio 0
	s_barrier
	s_mov_b32 m0, s81
	v_lshl_add_u64 v[142:143], s[44:45], 0, v[34:35]
	ds_read_b128 v[180:183], v146 offset:16384
	ds_read_b128 v[184:187], v146 offset:17408
	ds_read_b128 v[188:191], v146 offset:18432
	ds_read_b128 v[192:195], v146 offset:19456
	ds_read_b128 v[196:199], v146 offset:20480
	ds_read_b128 v[224:227], v146 offset:21504
	ds_read_b128 v[228:231], v146 offset:22528
	ds_read_b128 v[238:241], v146 offset:23552
	global_load_lds_dwordx4 v[142:143], off
	v_lshl_add_u64 v[212:213], s[44:45], 0, v[132:133]
	s_mov_b32 m0, s74
	v_lshl_add_u64 v[232:233], s[48:49], 0, v[34:35]
	global_load_lds_dwordx4 v[212:213], off
	s_mov_b32 m0, s80
	v_lshl_add_u64 v[242:243], s[46:47], 0, v[134:135]
	global_load_lds_dwordx4 v[232:233], off
	v_lshl_add_u64 v[232:233], s[48:49], 0, v[132:133]
	s_mov_b32 m0, s75
	s_nop 0
	global_load_lds_dwordx4 v[232:233], off
	v_lshl_add_u64 v[232:233], s[46:47], 0, v[138:139]
	s_mov_b32 m0, s52
	s_nop 0
	global_load_lds_dwordx4 v[232:233], off
	s_mov_b32 m0, s53
	s_nop 0
	global_load_lds_dwordx4 v[242:243], off
	s_waitcnt vmcnt(8)
	s_waitcnt lgkmcnt(0)
	s_barrier
	s_setprio 1
	s_waitcnt lgkmcnt(0)
	v_mfma_f32_16x16x32_bf16 v[64:67], v[148:151], v[180:183], v[64:67]
	v_mfma_f32_16x16x32_bf16 v[60:63], v[156:159], v[180:183], v[60:63]
	v_mfma_f32_16x16x32_bf16 v[56:59], v[148:151], v[188:191], v[56:59]
	v_mfma_f32_16x16x32_bf16 v[48:51], v[156:159], v[188:191], v[48:51]
	v_mfma_f32_16x16x32_bf16 v[40:43], v[148:151], v[196:199], v[40:43]
	v_mfma_f32_16x16x32_bf16 v[30:33], v[156:159], v[196:199], v[30:33]
	v_mfma_f32_16x16x32_bf16 v[22:25], v[148:151], v[228:231], v[22:25]
	v_mfma_f32_16x16x32_bf16 v[14:17], v[156:159], v[228:231], v[14:17]
	v_mfma_f32_16x16x32_bf16 v[64:67], v[152:155], v[184:187], v[64:67]
	v_mfma_f32_16x16x32_bf16 v[60:63], v[160:163], v[184:187], v[60:63]
	v_mfma_f32_16x16x32_bf16 v[56:59], v[152:155], v[192:195], v[56:59]
	v_mfma_f32_16x16x32_bf16 v[48:51], v[160:163], v[192:195], v[48:51]
	v_mfma_f32_16x16x32_bf16 v[40:43], v[152:155], v[224:227], v[40:43]
	v_mfma_f32_16x16x32_bf16 v[30:33], v[160:163], v[224:227], v[30:33]
	v_mfma_f32_16x16x32_bf16 v[22:25], v[152:155], v[238:241], v[22:25]
	v_mfma_f32_16x16x32_bf16 v[14:17], v[160:163], v[238:241], v[14:17]
	v_mfma_f32_16x16x32_bf16 v[52:55], v[164:167], v[180:183], v[52:55]
	v_mfma_f32_16x16x32_bf16 v[44:47], v[172:175], v[180:183], v[44:47]
	v_mfma_f32_16x16x32_bf16 v[36:39], v[164:167], v[188:191], v[36:39]
	v_mfma_f32_16x16x32_bf16 v[26:29], v[172:175], v[188:191], v[26:29]
	v_mfma_f32_16x16x32_bf16 v[18:21], v[164:167], v[196:199], v[18:21]
	v_mfma_f32_16x16x32_bf16 v[10:13], v[172:175], v[196:199], v[10:13]
	v_mfma_f32_16x16x32_bf16 v[6:9], v[164:167], v[228:231], v[6:9]
	v_mfma_f32_16x16x32_bf16 v[2:5], v[172:175], v[228:231], v[2:5]
	v_mfma_f32_16x16x32_bf16 v[52:55], v[168:171], v[184:187], v[52:55]
	v_mfma_f32_16x16x32_bf16 v[44:47], v[176:179], v[184:187], v[44:47]
	v_mfma_f32_16x16x32_bf16 v[36:39], v[168:171], v[192:195], v[36:39]
	v_mfma_f32_16x16x32_bf16 v[26:29], v[176:179], v[192:195], v[26:29]
	v_mfma_f32_16x16x32_bf16 v[18:21], v[168:171], v[224:227], v[18:21]
	v_mfma_f32_16x16x32_bf16 v[10:13], v[176:179], v[224:227], v[10:13]
	v_mfma_f32_16x16x32_bf16 v[6:9], v[168:171], v[238:241], v[6:9]
	v_mfma_f32_16x16x32_bf16 v[2:5], v[176:179], v[238:241], v[2:5]
	s_setprio 0
	s_barrier
	v_add_u32_e32 v147, s71, v144
	ds_read_b128 v[148:151], v147
	ds_read_b128 v[152:155], v147 offset:1024
	ds_read_b128 v[156:159], v147 offset:2048
	ds_read_b128 v[160:163], v147 offset:3072
	v_add_u32_e32 v147, s70, v144
	ds_read_b128 v[164:167], v147
	ds_read_b128 v[168:171], v147 offset:1024
	ds_read_b128 v[172:175], v147 offset:2048
	ds_read_b128 v[176:179], v147 offset:3072
	s_mov_b32 m0, s54
	v_lshl_add_u64 v[244:245], s[46:47], 0, v[140:141]
	ds_read_b128 v[180:183], v146 offset:32768
	ds_read_b128 v[184:187], v146 offset:33792
	ds_read_b128 v[188:191], v146 offset:34816
	ds_read_b128 v[192:195], v146 offset:35840
	ds_read_b128 v[196:199], v146 offset:36864
	ds_read_b128 v[224:227], v146 offset:37888
	ds_read_b128 v[228:231], v146 offset:38912
	ds_read_b128 v[238:241], v146 offset:39936
	global_load_lds_dwordx4 v[244:245], off
	v_lshl_add_u64 v[244:245], s[46:47], 0, v[136:137]
	s_mov_b32 m0, s55
	s_nop 0
	global_load_lds_dwordx4 v[244:245], off
	s_waitcnt vmcnt(8)
	s_waitcnt lgkmcnt(0)
	s_barrier
	s_setprio 1
	s_waitcnt lgkmcnt(0)
	v_mfma_f32_16x16x32_bf16 v[128:131], v[148:151], v[180:183], v[128:131]
	v_mfma_f32_16x16x32_bf16 v[124:127], v[156:159], v[180:183], v[124:127]
	v_mfma_f32_16x16x32_bf16 v[120:123], v[148:151], v[188:191], v[120:123]
	v_mfma_f32_16x16x32_bf16 v[112:115], v[156:159], v[188:191], v[112:115]
	v_mfma_f32_16x16x32_bf16 v[104:107], v[148:151], v[196:199], v[104:107]
	v_mfma_f32_16x16x32_bf16 v[96:99], v[156:159], v[196:199], v[96:99]
	v_mfma_f32_16x16x32_bf16 v[88:91], v[148:151], v[228:231], v[88:91]
	v_mfma_f32_16x16x32_bf16 v[80:83], v[156:159], v[228:231], v[80:83]
	v_mfma_f32_16x16x32_bf16 v[128:131], v[152:155], v[184:187], v[128:131]
	v_mfma_f32_16x16x32_bf16 v[124:127], v[160:163], v[184:187], v[124:127]
	v_mfma_f32_16x16x32_bf16 v[120:123], v[152:155], v[192:195], v[120:123]
	v_mfma_f32_16x16x32_bf16 v[112:115], v[160:163], v[192:195], v[112:115]
	v_mfma_f32_16x16x32_bf16 v[104:107], v[152:155], v[224:227], v[104:107]
	v_mfma_f32_16x16x32_bf16 v[96:99], v[160:163], v[224:227], v[96:99]
	v_mfma_f32_16x16x32_bf16 v[88:91], v[152:155], v[238:241], v[88:91]
	v_mfma_f32_16x16x32_bf16 v[80:83], v[160:163], v[238:241], v[80:83]
	v_mfma_f32_16x16x32_bf16 v[116:119], v[164:167], v[180:183], v[116:119]
	v_mfma_f32_16x16x32_bf16 v[108:111], v[172:175], v[180:183], v[108:111]
	v_mfma_f32_16x16x32_bf16 v[100:103], v[164:167], v[188:191], v[100:103]
	v_mfma_f32_16x16x32_bf16 v[92:95], v[172:175], v[188:191], v[92:95]
	v_mfma_f32_16x16x32_bf16 v[84:87], v[164:167], v[196:199], v[84:87]
	v_mfma_f32_16x16x32_bf16 v[76:79], v[172:175], v[196:199], v[76:79]
	v_mfma_f32_16x16x32_bf16 v[72:75], v[164:167], v[228:231], v[72:75]
	v_mfma_f32_16x16x32_bf16 v[68:71], v[172:175], v[228:231], v[68:71]
	v_mfma_f32_16x16x32_bf16 v[116:119], v[168:171], v[184:187], v[116:119]
	v_mfma_f32_16x16x32_bf16 v[108:111], v[176:179], v[184:187], v[108:111]
	v_mfma_f32_16x16x32_bf16 v[100:103], v[168:171], v[192:195], v[100:103]
	v_mfma_f32_16x16x32_bf16 v[92:95], v[176:179], v[192:195], v[92:95]
	v_mfma_f32_16x16x32_bf16 v[84:87], v[168:171], v[224:227], v[84:87]
	v_mfma_f32_16x16x32_bf16 v[76:79], v[176:179], v[224:227], v[76:79]
	v_mfma_f32_16x16x32_bf16 v[72:75], v[168:171], v[238:241], v[72:75]
	v_mfma_f32_16x16x32_bf16 v[68:71], v[176:179], v[238:241], v[68:71]
	s_setprio 0
	s_barrier
	s_mov_b32 m0, s27
	v_lshl_add_u64 v[142:143], v[142:143], 0, s[78:79]
	ds_read_b128 v[180:183], v146 offset:49152
	ds_read_b128 v[184:187], v146 offset:50176
	ds_read_b128 v[188:191], v146 offset:51200
	ds_read_b128 v[192:195], v146 offset:52224
	ds_read_b128 v[196:199], v146 offset:53248
	ds_read_b128 v[224:227], v146 offset:54272
	ds_read_b128 v[228:231], v146 offset:55296
	ds_read_b128 v[238:241], v146 offset:56320
	global_load_lds_dwordx4 v[142:143], off
	v_lshl_add_u64 v[142:143], v[212:213], 0, s[78:79]
	s_mov_b32 m0, s25
	s_nop 0
	global_load_lds_dwordx4 v[142:143], off
	v_lshl_add_u64 v[142:143], s[42:43], 0, v[34:35]
	s_mov_b32 m0, s83
	s_nop 0
	global_load_lds_dwordx4 v[142:143], off
	v_lshl_add_u64 v[142:143], s[42:43], 0, v[132:133]
	s_mov_b32 m0, s82
	s_nop 0
	global_load_lds_dwordx4 v[142:143], off
	v_lshl_add_u64 v[142:143], v[232:233], 0, s[78:79]
	s_mov_b32 m0, s56
	s_nop 0
	global_load_lds_dwordx4 v[142:143], off
	v_lshl_add_u64 v[142:143], v[242:243], 0, s[78:79]
	s_mov_b32 m0, s57
	s_nop 0
	global_load_lds_dwordx4 v[142:143], off
	s_waitcnt vmcnt(8)
	s_waitcnt lgkmcnt(0)
	s_barrier
	s_setprio 1
	s_waitcnt lgkmcnt(0)
	v_mfma_f32_16x16x32_bf16 v[64:67], v[148:151], v[180:183], v[64:67]
	v_mfma_f32_16x16x32_bf16 v[60:63], v[156:159], v[180:183], v[60:63]
	v_mfma_f32_16x16x32_bf16 v[56:59], v[148:151], v[188:191], v[56:59]
	v_mfma_f32_16x16x32_bf16 v[48:51], v[156:159], v[188:191], v[48:51]
	v_mfma_f32_16x16x32_bf16 v[40:43], v[148:151], v[196:199], v[40:43]
	v_mfma_f32_16x16x32_bf16 v[30:33], v[156:159], v[196:199], v[30:33]
	v_mfma_f32_16x16x32_bf16 v[22:25], v[148:151], v[228:231], v[22:25]
	v_mfma_f32_16x16x32_bf16 v[14:17], v[156:159], v[228:231], v[14:17]
	v_mfma_f32_16x16x32_bf16 v[64:67], v[152:155], v[184:187], v[64:67]
	v_mfma_f32_16x16x32_bf16 v[60:63], v[160:163], v[184:187], v[60:63]
	v_mfma_f32_16x16x32_bf16 v[56:59], v[152:155], v[192:195], v[56:59]
	v_mfma_f32_16x16x32_bf16 v[48:51], v[160:163], v[192:195], v[48:51]
	v_mfma_f32_16x16x32_bf16 v[40:43], v[152:155], v[224:227], v[40:43]
	v_mfma_f32_16x16x32_bf16 v[30:33], v[160:163], v[224:227], v[30:33]
	v_mfma_f32_16x16x32_bf16 v[22:25], v[152:155], v[238:241], v[22:25]
	v_mfma_f32_16x16x32_bf16 v[14:17], v[160:163], v[238:241], v[14:17]
	v_mfma_f32_16x16x32_bf16 v[52:55], v[164:167], v[180:183], v[52:55]
	v_mfma_f32_16x16x32_bf16 v[44:47], v[172:175], v[180:183], v[44:47]
	v_mfma_f32_16x16x32_bf16 v[36:39], v[164:167], v[188:191], v[36:39]
	v_mfma_f32_16x16x32_bf16 v[26:29], v[172:175], v[188:191], v[26:29]
	v_mfma_f32_16x16x32_bf16 v[18:21], v[164:167], v[196:199], v[18:21]
	v_mfma_f32_16x16x32_bf16 v[10:13], v[172:175], v[196:199], v[10:13]
	v_mfma_f32_16x16x32_bf16 v[6:9], v[164:167], v[228:231], v[6:9]
	v_mfma_f32_16x16x32_bf16 v[2:5], v[172:175], v[228:231], v[2:5]
	v_mfma_f32_16x16x32_bf16 v[52:55], v[168:171], v[184:187], v[52:55]
	v_mfma_f32_16x16x32_bf16 v[44:47], v[176:179], v[184:187], v[44:47]
	v_mfma_f32_16x16x32_bf16 v[36:39], v[168:171], v[192:195], v[36:39]
	v_mfma_f32_16x16x32_bf16 v[26:29], v[176:179], v[192:195], v[26:29]
	v_mfma_f32_16x16x32_bf16 v[18:21], v[168:171], v[224:227], v[18:21]
	v_mfma_f32_16x16x32_bf16 v[10:13], v[176:179], v[224:227], v[10:13]
	v_mfma_f32_16x16x32_bf16 v[6:9], v[168:171], v[238:241], v[6:9]
	v_mfma_f32_16x16x32_bf16 v[2:5], v[176:179], v[238:241], v[2:5]
	s_setprio 0
	s_barrier
	s_andn2_b64 vcc, exec, s[38:39]
	s_mov_b64 s[42:43], -1
	s_mov_b64 s[38:39], 0
	s_mov_b64 s[44:45], 0x100
	s_cbranch_vccz .LBB0_349
	s_and_b64 vcc, exec, s[22:23]
	s_cbranch_vccz .LBB0_352
	s_barrier

.LBB0_607:
	s_add_u32 s4, s30, 0x80
	s_addc_u32 s5, s31, 0
	s_add_i32 s53, 0, 0x10000
	s_cmp_eq_u32 s52, 28
	s_cselect_b32 s5, s27, s5
	s_cselect_b32 s4, s26, s4
	v_add_u32_e32 v153, s53, v150
	s_cselect_b32 s35, s29, s25
	s_cselect_b32 s34, s28, s23
	s_add_i32 s56, 0, 0x14000
	ds_read_b128 v[146:149], v153
	ds_read_b128 v[154:157], v153 offset:1024
	ds_read_b128 v[158:161], v153 offset:2048
	ds_read_b128 v[162:165], v153 offset:3072
	v_add_u32_e32 v153, s56, v150
	ds_read_b128 v[166:169], v153
	ds_read_b128 v[170:173], v153 offset:1024
	ds_read_b128 v[174:177], v153 offset:2048
	ds_read_b128 v[178:181], v153 offset:3072
	v_lshl_add_u64 v[198:199], s[30:31], 0, v[144:145]
	s_add_i32 m0, s42, 0xc000
	ds_read_b128 v[182:185], v152
	ds_read_b128 v[186:189], v152 offset:1024
	ds_read_b128 v[190:193], v152 offset:2048
	ds_read_b128 v[194:197], v152 offset:3072
	ds_read_b128 v[224:227], v152 offset:4096
	ds_read_b128 v[228:231], v152 offset:5120
	ds_read_b128 v[238:241], v152 offset:6144
	ds_read_b128 v[242:245], v152 offset:7168
	global_load_lds_dwordx4 v[198:199], off
	v_lshl_add_u64 v[198:199], s[30:31], 0, v[142:143]
	s_add_i32 m0, s42, 0xe000
	s_nop 0
	global_load_lds_dwordx4 v[198:199], off
	s_waitcnt vmcnt(8)
	s_waitcnt lgkmcnt(0)
	s_barrier
	s_setprio 1
	s_waitcnt lgkmcnt(0)
	v_mfma_f32_16x16x32_bf16 v[128:131], v[146:149], v[182:185], v[128:131]
	v_mfma_f32_16x16x32_bf16 v[124:127], v[158:161], v[182:185], v[124:127]
	v_mfma_f32_16x16x32_bf16 v[112:115], v[146:149], v[190:193], v[112:115]
	v_mfma_f32_16x16x32_bf16 v[108:111], v[158:161], v[190:193], v[108:111]
	v_mfma_f32_16x16x32_bf16 v[96:99], v[146:149], v[224:227], v[96:99]
	v_mfma_f32_16x16x32_bf16 v[92:95], v[158:161], v[224:227], v[92:95]
	v_mfma_f32_16x16x32_bf16 v[80:83], v[146:149], v[238:241], v[80:83]
	v_mfma_f32_16x16x32_bf16 v[76:79], v[158:161], v[238:241], v[76:79]
	v_mfma_f32_16x16x32_bf16 v[128:131], v[154:157], v[186:189], v[128:131]
	v_mfma_f32_16x16x32_bf16 v[124:127], v[162:165], v[186:189], v[124:127]
	v_mfma_f32_16x16x32_bf16 v[112:115], v[154:157], v[194:197], v[112:115]
	v_mfma_f32_16x16x32_bf16 v[108:111], v[162:165], v[194:197], v[108:111]
	v_mfma_f32_16x16x32_bf16 v[96:99], v[154:157], v[228:231], v[96:99]
	v_mfma_f32_16x16x32_bf16 v[92:95], v[162:165], v[228:231], v[92:95]
	v_mfma_f32_16x16x32_bf16 v[80:83], v[154:157], v[242:245], v[80:83]
	v_mfma_f32_16x16x32_bf16 v[76:79], v[162:165], v[242:245], v[76:79]
	v_mfma_f32_16x16x32_bf16 v[120:123], v[166:169], v[182:185], v[120:123]
	v_mfma_f32_16x16x32_bf16 v[116:119], v[174:177], v[182:185], v[116:119]
	v_mfma_f32_16x16x32_bf16 v[104:107], v[166:169], v[190:193], v[104:107]
	v_mfma_f32_16x16x32_bf16 v[100:103], v[174:177], v[190:193], v[100:103]
	v_mfma_f32_16x16x32_bf16 v[88:91], v[166:169], v[224:227], v[88:91]
	v_mfma_f32_16x16x32_bf16 v[84:87], v[174:177], v[224:227], v[84:87]
	v_mfma_f32_16x16x32_bf16 v[72:75], v[166:169], v[238:241], v[72:75]
	v_mfma_f32_16x16x32_bf16 v[68:71], v[174:177], v[238:241], v[68:71]
	v_mfma_f32_16x16x32_bf16 v[120:123], v[170:173], v[186:189], v[120:123]
	v_mfma_f32_16x16x32_bf16 v[116:119], v[178:181], v[186:189], v[116:119]
	v_mfma_f32_16x16x32_bf16 v[104:107], v[170:173], v[194:197], v[104:107]
	v_mfma_f32_16x16x32_bf16 v[100:103], v[178:181], v[194:197], v[100:103]
	v_mfma_f32_16x16x32_bf16 v[88:91], v[170:173], v[228:231], v[88:91]
	v_mfma_f32_16x16x32_bf16 v[84:87], v[178:181], v[228:231], v[84:87]
	v_mfma_f32_16x16x32_bf16 v[72:75], v[170:173], v[242:245], v[72:75]
	v_mfma_f32_16x16x32_bf16 v[68:71], v[178:181], v[242:245], v[68:71]
	s_setprio 0
	s_barrier
	s_add_i32 s53, s53, s39
	v_lshl_add_u64 v[198:199], s[34:35], 0, v[34:35]
	s_mov_b32 m0, s53
	ds_read_b128 v[182:185], v152 offset:16384
	ds_read_b128 v[186:189], v152 offset:17408
	ds_read_b128 v[190:193], v152 offset:18432
	ds_read_b128 v[194:197], v152 offset:19456
	ds_read_b128 v[224:227], v152 offset:20480
	ds_read_b128 v[228:231], v152 offset:21504
	ds_read_b128 v[238:241], v152 offset:22528
	ds_read_b128 v[242:245], v152 offset:23552
	global_load_lds_dwordx4 v[198:199], off
	s_add_i32 m0, s53, 0x2000
	s_add_u32 s54, s34, 0x80000
	v_lshl_add_u64 v[212:213], s[34:35], 0, v[132:133]
	s_addc_u32 s55, s35, 0
	s_add_i32 s53, s56, s39
	global_load_lds_dwordx4 v[212:213], off
	v_lshl_add_u64 v[232:233], s[54:55], 0, v[34:35]
	s_mov_b32 m0, s53
	v_lshl_add_u64 v[246:247], s[4:5], 0, v[134:135]
	global_load_lds_dwordx4 v[232:233], off
	v_lshl_add_u64 v[232:233], s[54:55], 0, v[132:133]
	s_add_i32 m0, s53, 0x2000
	s_nop 0
	global_load_lds_dwordx4 v[232:233], off
	v_lshl_add_u64 v[232:233], s[4:5], 0, v[138:139]
	s_mov_b32 m0, s42
	s_nop 0
	global_load_lds_dwordx4 v[232:233], off
	s_mov_b32 m0, s43
	s_nop 0
	global_load_lds_dwordx4 v[246:247], off
	s_waitcnt vmcnt(8)
	s_waitcnt lgkmcnt(0)
	s_barrier
	s_setprio 1
	s_waitcnt lgkmcnt(0)
	v_mfma_f32_16x16x32_bf16 v[64:67], v[146:149], v[182:185], v[64:67]
	v_mfma_f32_16x16x32_bf16 v[60:63], v[158:161], v[182:185], v[60:63]
	v_mfma_f32_16x16x32_bf16 v[48:51], v[146:149], v[190:193], v[48:51]
	v_mfma_f32_16x16x32_bf16 v[44:47], v[158:161], v[190:193], v[44:47]
	v_mfma_f32_16x16x32_bf16 v[30:33], v[146:149], v[224:227], v[30:33]
	v_mfma_f32_16x16x32_bf16 v[26:29], v[158:161], v[224:227], v[26:29]
	v_mfma_f32_16x16x32_bf16 v[14:17], v[146:149], v[238:241], v[14:17]
	v_mfma_f32_16x16x32_bf16 v[10:13], v[158:161], v[238:241], v[10:13]
	v_mfma_f32_16x16x32_bf16 v[64:67], v[154:157], v[186:189], v[64:67]
	v_mfma_f32_16x16x32_bf16 v[60:63], v[162:165], v[186:189], v[60:63]
	v_mfma_f32_16x16x32_bf16 v[48:51], v[154:157], v[194:197], v[48:51]
	v_mfma_f32_16x16x32_bf16 v[44:47], v[162:165], v[194:197], v[44:47]
	v_mfma_f32_16x16x32_bf16 v[30:33], v[154:157], v[228:231], v[30:33]
	v_mfma_f32_16x16x32_bf16 v[26:29], v[162:165], v[228:231], v[26:29]
	v_mfma_f32_16x16x32_bf16 v[14:17], v[154:157], v[242:245], v[14:17]
	v_mfma_f32_16x16x32_bf16 v[10:13], v[162:165], v[242:245], v[10:13]
	v_mfma_f32_16x16x32_bf16 v[56:59], v[166:169], v[182:185], v[56:59]
	v_mfma_f32_16x16x32_bf16 v[52:55], v[174:177], v[182:185], v[52:55]
	v_mfma_f32_16x16x32_bf16 v[40:43], v[166:169], v[190:193], v[40:43]
	v_mfma_f32_16x16x32_bf16 v[36:39], v[174:177], v[190:193], v[36:39]
	v_mfma_f32_16x16x32_bf16 v[22:25], v[166:169], v[224:227], v[22:25]
	v_mfma_f32_16x16x32_bf16 v[18:21], v[174:177], v[224:227], v[18:21]
	v_mfma_f32_16x16x32_bf16 v[6:9], v[166:169], v[238:241], v[6:9]
	v_mfma_f32_16x16x32_bf16 v[2:5], v[174:177], v[238:241], v[2:5]
	v_mfma_f32_16x16x32_bf16 v[56:59], v[170:173], v[186:189], v[56:59]
	v_mfma_f32_16x16x32_bf16 v[52:55], v[178:181], v[186:189], v[52:55]
	v_mfma_f32_16x16x32_bf16 v[40:43], v[170:173], v[194:197], v[40:43]
	v_mfma_f32_16x16x32_bf16 v[36:39], v[178:181], v[194:197], v[36:39]
	v_mfma_f32_16x16x32_bf16 v[22:25], v[170:173], v[228:231], v[22:25]
	v_mfma_f32_16x16x32_bf16 v[18:21], v[178:181], v[228:231], v[18:21]
	v_mfma_f32_16x16x32_bf16 v[6:9], v[170:173], v[242:245], v[6:9]
	v_mfma_f32_16x16x32_bf16 v[2:5], v[178:181], v[242:245], v[2:5]
	s_setprio 0
	s_barrier
	s_add_i32 s53, 0, 0x18000
	v_add_u32_e32 v153, s53, v150
	s_add_i32 s54, 0, 0x1c000
	ds_read_b128 v[146:149], v153
	ds_read_b128 v[154:157], v153 offset:1024
	ds_read_b128 v[158:161], v153 offset:2048
	ds_read_b128 v[162:165], v153 offset:3072
	v_add_u32_e32 v153, s54, v150
	ds_read_b128 v[166:169], v153
	ds_read_b128 v[170:173], v153 offset:1024
	ds_read_b128 v[174:177], v153 offset:2048
	ds_read_b128 v[178:181], v153 offset:3072
	s_mov_b32 m0, s44
	v_lshl_add_u64 v[248:249], s[4:5], 0, v[140:141]
	ds_read_b128 v[182:185], v152 offset:32768
	ds_read_b128 v[186:189], v152 offset:33792
	ds_read_b128 v[190:193], v152 offset:34816
	ds_read_b128 v[194:197], v152 offset:35840
	ds_read_b128 v[224:227], v152 offset:36864
	ds_read_b128 v[228:231], v152 offset:37888
	ds_read_b128 v[238:241], v152 offset:38912
	ds_read_b128 v[242:245], v152 offset:39936
	global_load_lds_dwordx4 v[248:249], off
	v_lshl_add_u64 v[248:249], s[4:5], 0, v[136:137]
	s_mov_b32 m0, s45
	s_nop 0
	global_load_lds_dwordx4 v[248:249], off
	s_waitcnt vmcnt(8)
	s_waitcnt lgkmcnt(0)
	s_barrier
	s_setprio 1
	s_waitcnt lgkmcnt(0)
	v_mfma_f32_16x16x32_bf16 v[128:131], v[146:149], v[182:185], v[128:131]
	v_mfma_f32_16x16x32_bf16 v[124:127], v[158:161], v[182:185], v[124:127]
	v_mfma_f32_16x16x32_bf16 v[112:115], v[146:149], v[190:193], v[112:115]
	v_mfma_f32_16x16x32_bf16 v[108:111], v[158:161], v[190:193], v[108:111]
	v_mfma_f32_16x16x32_bf16 v[96:99], v[146:149], v[224:227], v[96:99]
	v_mfma_f32_16x16x32_bf16 v[92:95], v[158:161], v[224:227], v[92:95]
	v_mfma_f32_16x16x32_bf16 v[80:83], v[146:149], v[238:241], v[80:83]
	v_mfma_f32_16x16x32_bf16 v[76:79], v[158:161], v[238:241], v[76:79]
	v_mfma_f32_16x16x32_bf16 v[128:131], v[154:157], v[186:189], v[128:131]
	v_mfma_f32_16x16x32_bf16 v[124:127], v[162:165], v[186:189], v[124:127]
	v_mfma_f32_16x16x32_bf16 v[112:115], v[154:157], v[194:197], v[112:115]
	v_mfma_f32_16x16x32_bf16 v[108:111], v[162:165], v[194:197], v[108:111]
	v_mfma_f32_16x16x32_bf16 v[96:99], v[154:157], v[228:231], v[96:99]
	v_mfma_f32_16x16x32_bf16 v[92:95], v[162:165], v[228:231], v[92:95]
	v_mfma_f32_16x16x32_bf16 v[80:83], v[154:157], v[242:245], v[80:83]
	v_mfma_f32_16x16x32_bf16 v[76:79], v[162:165], v[242:245], v[76:79]
	v_mfma_f32_16x16x32_bf16 v[120:123], v[166:169], v[182:185], v[120:123]
	v_mfma_f32_16x16x32_bf16 v[116:119], v[174:177], v[182:185], v[116:119]
	v_mfma_f32_16x16x32_bf16 v[104:107], v[166:169], v[190:193], v[104:107]
	v_mfma_f32_16x16x32_bf16 v[100:103], v[174:177], v[190:193], v[100:103]
	v_mfma_f32_16x16x32_bf16 v[88:91], v[166:169], v[224:227], v[88:91]
	v_mfma_f32_16x16x32_bf16 v[84:87], v[174:177], v[224:227], v[84:87]
	v_mfma_f32_16x16x32_bf16 v[72:75], v[166:169], v[238:241], v[72:75]
	v_mfma_f32_16x16x32_bf16 v[68:71], v[174:177], v[238:241], v[68:71]
	v_mfma_f32_16x16x32_bf16 v[120:123], v[170:173], v[186:189], v[120:123]
	v_mfma_f32_16x16x32_bf16 v[116:119], v[178:181], v[186:189], v[116:119]
	v_mfma_f32_16x16x32_bf16 v[104:107], v[170:173], v[194:197], v[104:107]
	v_mfma_f32_16x16x32_bf16 v[100:103], v[178:181], v[194:197], v[100:103]
	v_mfma_f32_16x16x32_bf16 v[88:91], v[170:173], v[228:231], v[88:91]
	v_mfma_f32_16x16x32_bf16 v[84:87], v[178:181], v[228:231], v[84:87]
	v_mfma_f32_16x16x32_bf16 v[72:75], v[170:173], v[242:245], v[72:75]
	v_mfma_f32_16x16x32_bf16 v[68:71], v[178:181], v[242:245], v[68:71]
	s_setprio 0
	s_barrier
	s_add_i32 s4, s53, s39
	v_lshl_add_u64 v[198:199], v[198:199], 0, s[78:79]
	s_mov_b32 m0, s4
	ds_read_b128 v[182:185], v152 offset:49152
	ds_read_b128 v[186:189], v152 offset:50176
	ds_read_b128 v[190:193], v152 offset:51200
	ds_read_b128 v[194:197], v152 offset:52224
	ds_read_b128 v[224:227], v152 offset:53248
	ds_read_b128 v[228:231], v152 offset:54272
	ds_read_b128 v[238:241], v152 offset:55296
	ds_read_b128 v[242:245], v152 offset:56320
	global_load_lds_dwordx4 v[198:199], off
	s_add_i32 m0, s4, 0x2000
	s_add_u32 s4, s34, 0x80080
	v_lshl_add_u64 v[198:199], v[212:213], 0, s[78:79]
	s_addc_u32 s5, s35, 0
	s_add_i32 s34, s54, s39
	global_load_lds_dwordx4 v[198:199], off
	v_lshl_add_u64 v[198:199], s[4:5], 0, v[34:35]
	s_mov_b32 m0, s34
	s_nop 0
	global_load_lds_dwordx4 v[198:199], off
	v_lshl_add_u64 v[198:199], s[4:5], 0, v[132:133]
	s_add_i32 m0, s34, 0x2000
	s_nop 0
	global_load_lds_dwordx4 v[198:199], off
	v_lshl_add_u64 v[198:199], v[232:233], 0, s[78:79]
	s_mov_b32 m0, s46
	s_nop 0
	global_load_lds_dwordx4 v[198:199], off
	v_lshl_add_u64 v[198:199], v[246:247], 0, s[78:79]
	s_mov_b32 m0, s47
	s_nop 0
	global_load_lds_dwordx4 v[198:199], off
	s_waitcnt vmcnt(8)
	s_waitcnt lgkmcnt(0)
	s_barrier
	s_setprio 1
	s_waitcnt lgkmcnt(0)
	v_mfma_f32_16x16x32_bf16 v[64:67], v[146:149], v[182:185], v[64:67]
	v_mfma_f32_16x16x32_bf16 v[60:63], v[158:161], v[182:185], v[60:63]
	v_mfma_f32_16x16x32_bf16 v[48:51], v[146:149], v[190:193], v[48:51]
	v_mfma_f32_16x16x32_bf16 v[44:47], v[158:161], v[190:193], v[44:47]
	v_mfma_f32_16x16x32_bf16 v[30:33], v[146:149], v[224:227], v[30:33]
	v_mfma_f32_16x16x32_bf16 v[26:29], v[158:161], v[224:227], v[26:29]
	v_mfma_f32_16x16x32_bf16 v[14:17], v[146:149], v[238:241], v[14:17]
	v_mfma_f32_16x16x32_bf16 v[10:13], v[158:161], v[238:241], v[10:13]
	v_mfma_f32_16x16x32_bf16 v[64:67], v[154:157], v[186:189], v[64:67]
	v_mfma_f32_16x16x32_bf16 v[60:63], v[162:165], v[186:189], v[60:63]
	v_mfma_f32_16x16x32_bf16 v[48:51], v[154:157], v[194:197], v[48:51]
	v_mfma_f32_16x16x32_bf16 v[44:47], v[162:165], v[194:197], v[44:47]
	v_mfma_f32_16x16x32_bf16 v[30:33], v[154:157], v[228:231], v[30:33]
	v_mfma_f32_16x16x32_bf16 v[26:29], v[162:165], v[228:231], v[26:29]
	v_mfma_f32_16x16x32_bf16 v[14:17], v[154:157], v[242:245], v[14:17]
	v_mfma_f32_16x16x32_bf16 v[10:13], v[162:165], v[242:245], v[10:13]
	v_mfma_f32_16x16x32_bf16 v[56:59], v[166:169], v[182:185], v[56:59]
	v_mfma_f32_16x16x32_bf16 v[52:55], v[174:177], v[182:185], v[52:55]
	v_mfma_f32_16x16x32_bf16 v[40:43], v[166:169], v[190:193], v[40:43]
	v_mfma_f32_16x16x32_bf16 v[36:39], v[174:177], v[190:193], v[36:39]
	v_mfma_f32_16x16x32_bf16 v[22:25], v[166:169], v[224:227], v[22:25]
	v_mfma_f32_16x16x32_bf16 v[18:21], v[174:177], v[224:227], v[18:21]
	v_mfma_f32_16x16x32_bf16 v[6:9], v[166:169], v[238:241], v[6:9]
	v_mfma_f32_16x16x32_bf16 v[2:5], v[174:177], v[238:241], v[2:5]
	v_mfma_f32_16x16x32_bf16 v[56:59], v[170:173], v[186:189], v[56:59]
	v_mfma_f32_16x16x32_bf16 v[52:55], v[178:181], v[186:189], v[52:55]
	v_mfma_f32_16x16x32_bf16 v[40:43], v[170:173], v[194:197], v[40:43]
	v_mfma_f32_16x16x32_bf16 v[36:39], v[178:181], v[194:197], v[36:39]
	v_mfma_f32_16x16x32_bf16 v[22:25], v[170:173], v[228:231], v[22:25]
	v_mfma_f32_16x16x32_bf16 v[18:21], v[178:181], v[228:231], v[18:21]
	v_mfma_f32_16x16x32_bf16 v[6:9], v[170:173], v[242:245], v[6:9]
	v_mfma_f32_16x16x32_bf16 v[2:5], v[178:181], v[242:245], v[2:5]
	s_setprio 0
	s_barrier
	s_add_i32 s52, s52, 2
	s_add_u32 s23, s23, 0x100
	s_addc_u32 s25, s25, 0
	s_add_u32 s30, s30, 0x100
	s_addc_u32 s31, s31, 0
	s_cmp_gt_u32 s52, 29
	s_cbranch_scc0 .LBB0_607
	s_and_b64 vcc, exec, s[20:21]
	s_cbranch_vccz .LBB0_610
	s_barrier

.LBB0_673:
	s_add_u32 s4, s30, 0x80
	s_addc_u32 s5, s31, 0
	s_add_i32 s64, 0, 0x10000
	s_cmp_eq_u32 s57, 12
	s_cselect_b32 s5, s27, s5
	s_cselect_b32 s4, s26, s4
	s_cselect_b32 s35, s29, s25
	s_cselect_b32 s34, s28, s23
	s_add_i32 s68, 0, 0x14000
	v_add_u32_e32 v144, s64, v190
	v_add_u32_e32 v160, s68, v190
	ds_read_b128 v[132:135], v144
	ds_read_b128 v[136:139], v144 offset:1024
	ds_read_b128 v[140:143], v144 offset:2048
	ds_read_b128 v[144:147], v144 offset:3072
	ds_read_b128 v[148:151], v160
	ds_read_b128 v[152:155], v160 offset:1024
	ds_read_b128 v[156:159], v160 offset:2048
	ds_read_b128 v[160:163], v160 offset:3072
	v_lshl_add_u64 v[164:165], s[30:31], 0, v[178:179]
	s_add_i32 m0, s38, 0xc000
	ds_read_b128 v[180:183], v192
	ds_read_b128 v[184:187], v192 offset:1024
	ds_read_b128 v[194:197], v192 offset:2048
	ds_read_b128 v[224:227], v192 offset:3072
	ds_read_b128 v[228:231], v192 offset:4096
	ds_read_b128 v[238:241], v192 offset:5120
	ds_read_b128 v[242:245], v192 offset:6144
	ds_read_b128 v[246:249], v192 offset:7168
	global_load_lds_dwordx4 v[164:165], off
	v_lshl_add_u64 v[164:165], s[30:31], 0, v[176:177]
	s_add_i32 m0, s38, 0xe000
	s_nop 0
	global_load_lds_dwordx4 v[164:165], off
	s_waitcnt vmcnt(8)
	s_waitcnt lgkmcnt(0)
	s_barrier
	s_setprio 1
	s_waitcnt lgkmcnt(0)
	v_mfma_f32_16x16x32_bf16 v[128:131], v[132:135], v[180:183], v[128:131]
	v_mfma_f32_16x16x32_bf16 v[124:127], v[140:143], v[180:183], v[124:127]
	v_mfma_f32_16x16x32_bf16 v[112:115], v[132:135], v[194:197], v[112:115]
	v_mfma_f32_16x16x32_bf16 v[108:111], v[140:143], v[194:197], v[108:111]
	v_mfma_f32_16x16x32_bf16 v[96:99], v[132:135], v[228:231], v[96:99]
	v_mfma_f32_16x16x32_bf16 v[92:95], v[140:143], v[228:231], v[92:95]
	v_mfma_f32_16x16x32_bf16 v[80:83], v[132:135], v[242:245], v[80:83]
	v_mfma_f32_16x16x32_bf16 v[76:79], v[140:143], v[242:245], v[76:79]
	v_mfma_f32_16x16x32_bf16 v[128:131], v[136:139], v[184:187], v[128:131]
	v_mfma_f32_16x16x32_bf16 v[124:127], v[144:147], v[184:187], v[124:127]
	v_mfma_f32_16x16x32_bf16 v[112:115], v[136:139], v[224:227], v[112:115]
	v_mfma_f32_16x16x32_bf16 v[108:111], v[144:147], v[224:227], v[108:111]
	v_mfma_f32_16x16x32_bf16 v[96:99], v[136:139], v[238:241], v[96:99]
	v_mfma_f32_16x16x32_bf16 v[92:95], v[144:147], v[238:241], v[92:95]
	v_mfma_f32_16x16x32_bf16 v[80:83], v[136:139], v[246:249], v[80:83]
	v_mfma_f32_16x16x32_bf16 v[76:79], v[144:147], v[246:249], v[76:79]
	v_mfma_f32_16x16x32_bf16 v[120:123], v[148:151], v[180:183], v[120:123]
	v_mfma_f32_16x16x32_bf16 v[116:119], v[156:159], v[180:183], v[116:119]
	v_mfma_f32_16x16x32_bf16 v[104:107], v[148:151], v[194:197], v[104:107]
	v_mfma_f32_16x16x32_bf16 v[100:103], v[156:159], v[194:197], v[100:103]
	v_mfma_f32_16x16x32_bf16 v[88:91], v[148:151], v[228:231], v[88:91]
	v_mfma_f32_16x16x32_bf16 v[84:87], v[156:159], v[228:231], v[84:87]
	v_mfma_f32_16x16x32_bf16 v[72:75], v[148:151], v[242:245], v[72:75]
	v_mfma_f32_16x16x32_bf16 v[68:71], v[156:159], v[242:245], v[68:71]
	v_mfma_f32_16x16x32_bf16 v[120:123], v[152:155], v[184:187], v[120:123]
	v_mfma_f32_16x16x32_bf16 v[116:119], v[160:163], v[184:187], v[116:119]
	v_mfma_f32_16x16x32_bf16 v[104:107], v[152:155], v[224:227], v[104:107]
	v_mfma_f32_16x16x32_bf16 v[100:103], v[160:163], v[224:227], v[100:103]
	v_mfma_f32_16x16x32_bf16 v[88:91], v[152:155], v[238:241], v[88:91]
	v_mfma_f32_16x16x32_bf16 v[84:87], v[160:163], v[238:241], v[84:87]
	v_mfma_f32_16x16x32_bf16 v[72:75], v[152:155], v[246:249], v[72:75]
	v_mfma_f32_16x16x32_bf16 v[68:71], v[160:163], v[246:249], v[68:71]
	s_setprio 0
	s_barrier
	s_add_i32 s64, s64, s37
	v_lshl_add_u64 v[164:165], s[34:35], 0, v[34:35]
	s_mov_b32 m0, s64
	ds_read_b128 v[180:183], v192 offset:16384
	ds_read_b128 v[184:187], v192 offset:17408
	ds_read_b128 v[194:197], v192 offset:18432
	ds_read_b128 v[224:227], v192 offset:19456
	ds_read_b128 v[228:231], v192 offset:20480
	ds_read_b128 v[238:241], v192 offset:21504
	ds_read_b128 v[242:245], v192 offset:22528
	ds_read_b128 v[246:249], v192 offset:23552
	global_load_lds_dwordx4 v[164:165], off
	s_add_i32 m0, s64, 0x2000
	s_add_u32 s64, s34, 0x40000
	v_lshl_add_u64 v[188:189], s[34:35], 0, v[174:175]
	s_addc_u32 s65, s35, 0
	s_add_i32 s68, s68, s37
	global_load_lds_dwordx4 v[188:189], off
	v_lshl_add_u64 v[198:199], s[64:65], 0, v[34:35]
	s_mov_b32 m0, s68
	v_lshl_add_u64 v[212:213], s[4:5], 0, v[170:171]
	global_load_lds_dwordx4 v[198:199], off
	v_lshl_add_u64 v[198:199], s[64:65], 0, v[174:175]
	s_add_i32 m0, s68, 0x2000
	s_nop 0
	global_load_lds_dwordx4 v[198:199], off
	v_lshl_add_u64 v[198:199], s[4:5], 0, v[166:167]
	s_mov_b32 m0, s38
	s_nop 0
	global_load_lds_dwordx4 v[198:199], off
	s_mov_b32 m0, s39
	s_nop 0
	global_load_lds_dwordx4 v[212:213], off
	s_waitcnt vmcnt(8)
	s_waitcnt lgkmcnt(0)
	s_barrier
	s_setprio 1
	s_waitcnt lgkmcnt(0)
	v_mfma_f32_16x16x32_bf16 v[64:67], v[132:135], v[180:183], v[64:67]
	v_mfma_f32_16x16x32_bf16 v[60:63], v[140:143], v[180:183], v[60:63]
	v_mfma_f32_16x16x32_bf16 v[48:51], v[132:135], v[194:197], v[48:51]
	v_mfma_f32_16x16x32_bf16 v[44:47], v[140:143], v[194:197], v[44:47]
	v_mfma_f32_16x16x32_bf16 v[30:33], v[132:135], v[228:231], v[30:33]
	v_mfma_f32_16x16x32_bf16 v[26:29], v[140:143], v[228:231], v[26:29]
	v_mfma_f32_16x16x32_bf16 v[14:17], v[132:135], v[242:245], v[14:17]
	v_mfma_f32_16x16x32_bf16 v[10:13], v[140:143], v[242:245], v[10:13]
	v_mfma_f32_16x16x32_bf16 v[64:67], v[136:139], v[184:187], v[64:67]
	v_mfma_f32_16x16x32_bf16 v[60:63], v[144:147], v[184:187], v[60:63]
	v_mfma_f32_16x16x32_bf16 v[48:51], v[136:139], v[224:227], v[48:51]
	v_mfma_f32_16x16x32_bf16 v[44:47], v[144:147], v[224:227], v[44:47]
	v_mfma_f32_16x16x32_bf16 v[30:33], v[136:139], v[238:241], v[30:33]
	v_mfma_f32_16x16x32_bf16 v[26:29], v[144:147], v[238:241], v[26:29]
	v_mfma_f32_16x16x32_bf16 v[14:17], v[136:139], v[246:249], v[14:17]
	v_mfma_f32_16x16x32_bf16 v[10:13], v[144:147], v[246:249], v[10:13]
	v_mfma_f32_16x16x32_bf16 v[56:59], v[148:151], v[180:183], v[56:59]
	v_mfma_f32_16x16x32_bf16 v[52:55], v[156:159], v[180:183], v[52:55]
	v_mfma_f32_16x16x32_bf16 v[40:43], v[148:151], v[194:197], v[40:43]
	v_mfma_f32_16x16x32_bf16 v[36:39], v[156:159], v[194:197], v[36:39]
	v_mfma_f32_16x16x32_bf16 v[22:25], v[148:151], v[228:231], v[22:25]
	v_mfma_f32_16x16x32_bf16 v[18:21], v[156:159], v[228:231], v[18:21]
	v_mfma_f32_16x16x32_bf16 v[6:9], v[148:151], v[242:245], v[6:9]
	v_mfma_f32_16x16x32_bf16 v[2:5], v[156:159], v[242:245], v[2:5]
	v_mfma_f32_16x16x32_bf16 v[56:59], v[152:155], v[184:187], v[56:59]
	v_mfma_f32_16x16x32_bf16 v[52:55], v[160:163], v[184:187], v[52:55]
	v_mfma_f32_16x16x32_bf16 v[40:43], v[152:155], v[224:227], v[40:43]
	v_mfma_f32_16x16x32_bf16 v[36:39], v[160:163], v[224:227], v[36:39]
	v_mfma_f32_16x16x32_bf16 v[22:25], v[152:155], v[238:241], v[22:25]
	v_mfma_f32_16x16x32_bf16 v[18:21], v[160:163], v[238:241], v[18:21]
	v_mfma_f32_16x16x32_bf16 v[6:9], v[152:155], v[246:249], v[6:9]
	v_mfma_f32_16x16x32_bf16 v[2:5], v[160:163], v[246:249], v[2:5]
	s_setprio 0
	s_barrier
	s_add_i32 s64, 0, 0x18000
	s_add_i32 s65, 0, 0x1c000
	v_add_u32_e32 v144, s64, v190
	v_add_u32_e32 v160, s65, v190
	ds_read_b128 v[132:135], v144
	ds_read_b128 v[136:139], v144 offset:1024
	ds_read_b128 v[140:143], v144 offset:2048
	ds_read_b128 v[144:147], v144 offset:3072
	ds_read_b128 v[148:151], v160
	ds_read_b128 v[152:155], v160 offset:1024
	ds_read_b128 v[156:159], v160 offset:2048
	ds_read_b128 v[160:163], v160 offset:3072
	s_mov_b32 m0, s46
	v_lshl_add_u64 v[232:233], s[4:5], 0, v[168:169]
	ds_read_b128 v[180:183], v192 offset:32768
	ds_read_b128 v[184:187], v192 offset:33792
	ds_read_b128 v[194:197], v192 offset:34816
	ds_read_b128 v[224:227], v192 offset:35840
	ds_read_b128 v[228:231], v192 offset:36864
	ds_read_b128 v[238:241], v192 offset:37888
	ds_read_b128 v[242:245], v192 offset:38912
	ds_read_b128 v[246:249], v192 offset:39936
	global_load_lds_dwordx4 v[232:233], off
	v_lshl_add_u64 v[232:233], s[4:5], 0, v[172:173]
	s_mov_b32 m0, s47
	s_nop 0
	global_load_lds_dwordx4 v[232:233], off
	s_waitcnt vmcnt(8)
	s_waitcnt lgkmcnt(0)
	s_barrier
	s_setprio 1
	s_waitcnt lgkmcnt(0)
	v_mfma_f32_16x16x32_bf16 v[128:131], v[132:135], v[180:183], v[128:131]
	v_mfma_f32_16x16x32_bf16 v[124:127], v[140:143], v[180:183], v[124:127]
	v_mfma_f32_16x16x32_bf16 v[112:115], v[132:135], v[194:197], v[112:115]
	v_mfma_f32_16x16x32_bf16 v[108:111], v[140:143], v[194:197], v[108:111]
	v_mfma_f32_16x16x32_bf16 v[96:99], v[132:135], v[228:231], v[96:99]
	v_mfma_f32_16x16x32_bf16 v[92:95], v[140:143], v[228:231], v[92:95]
	v_mfma_f32_16x16x32_bf16 v[80:83], v[132:135], v[242:245], v[80:83]
	v_mfma_f32_16x16x32_bf16 v[76:79], v[140:143], v[242:245], v[76:79]
	v_mfma_f32_16x16x32_bf16 v[128:131], v[136:139], v[184:187], v[128:131]
	v_mfma_f32_16x16x32_bf16 v[124:127], v[144:147], v[184:187], v[124:127]
	v_mfma_f32_16x16x32_bf16 v[112:115], v[136:139], v[224:227], v[112:115]
	v_mfma_f32_16x16x32_bf16 v[108:111], v[144:147], v[224:227], v[108:111]
	v_mfma_f32_16x16x32_bf16 v[96:99], v[136:139], v[238:241], v[96:99]
	v_mfma_f32_16x16x32_bf16 v[92:95], v[144:147], v[238:241], v[92:95]
	v_mfma_f32_16x16x32_bf16 v[80:83], v[136:139], v[246:249], v[80:83]
	v_mfma_f32_16x16x32_bf16 v[76:79], v[144:147], v[246:249], v[76:79]
	v_mfma_f32_16x16x32_bf16 v[120:123], v[148:151], v[180:183], v[120:123]
	v_mfma_f32_16x16x32_bf16 v[116:119], v[156:159], v[180:183], v[116:119]
	v_mfma_f32_16x16x32_bf16 v[104:107], v[148:151], v[194:197], v[104:107]
	v_mfma_f32_16x16x32_bf16 v[100:103], v[156:159], v[194:197], v[100:103]
	v_mfma_f32_16x16x32_bf16 v[88:91], v[148:151], v[228:231], v[88:91]
	v_mfma_f32_16x16x32_bf16 v[84:87], v[156:159], v[228:231], v[84:87]
	v_mfma_f32_16x16x32_bf16 v[72:75], v[148:151], v[242:245], v[72:75]
	v_mfma_f32_16x16x32_bf16 v[68:71], v[156:159], v[242:245], v[68:71]
	v_mfma_f32_16x16x32_bf16 v[120:123], v[152:155], v[184:187], v[120:123]
	v_mfma_f32_16x16x32_bf16 v[116:119], v[160:163], v[184:187], v[116:119]
	v_mfma_f32_16x16x32_bf16 v[104:107], v[152:155], v[224:227], v[104:107]
	v_mfma_f32_16x16x32_bf16 v[100:103], v[160:163], v[224:227], v[100:103]
	v_mfma_f32_16x16x32_bf16 v[88:91], v[152:155], v[238:241], v[88:91]
	v_mfma_f32_16x16x32_bf16 v[84:87], v[160:163], v[238:241], v[84:87]
	v_mfma_f32_16x16x32_bf16 v[72:75], v[152:155], v[246:249], v[72:75]
	v_mfma_f32_16x16x32_bf16 v[68:71], v[160:163], v[246:249], v[68:71]
	s_setprio 0
	s_barrier
	s_add_i32 s4, s64, s37
	v_lshl_add_u64 v[164:165], v[164:165], 0, s[78:79]
	s_mov_b32 m0, s4
	ds_read_b128 v[180:183], v192 offset:49152
	ds_read_b128 v[184:187], v192 offset:50176
	ds_read_b128 v[194:197], v192 offset:51200
	ds_read_b128 v[224:227], v192 offset:52224
	ds_read_b128 v[228:231], v192 offset:53248
	ds_read_b128 v[238:241], v192 offset:54272
	ds_read_b128 v[242:245], v192 offset:55296
	ds_read_b128 v[246:249], v192 offset:56320
	global_load_lds_dwordx4 v[164:165], off
	s_add_i32 m0, s4, 0x2000
	s_add_u32 s4, s34, 0x40080
	v_lshl_add_u64 v[164:165], v[188:189], 0, s[78:79]
	s_addc_u32 s5, s35, 0
	s_add_i32 s34, s65, s37
	global_load_lds_dwordx4 v[164:165], off
	v_lshl_add_u64 v[164:165], s[4:5], 0, v[34:35]
	s_mov_b32 m0, s34
	s_nop 0
	global_load_lds_dwordx4 v[164:165], off
	v_lshl_add_u64 v[164:165], s[4:5], 0, v[174:175]
	s_add_i32 m0, s34, 0x2000
	s_nop 0
	global_load_lds_dwordx4 v[164:165], off
	v_lshl_add_u64 v[164:165], v[198:199], 0, s[78:79]
	s_mov_b32 m0, s52
	s_nop 0
	global_load_lds_dwordx4 v[164:165], off
	v_lshl_add_u64 v[164:165], v[212:213], 0, s[78:79]
	s_mov_b32 m0, s53
	s_nop 0
	global_load_lds_dwordx4 v[164:165], off
	s_waitcnt vmcnt(8)
	s_waitcnt lgkmcnt(0)
	s_barrier
	s_setprio 1
	s_waitcnt lgkmcnt(0)
	v_mfma_f32_16x16x32_bf16 v[64:67], v[132:135], v[180:183], v[64:67]
	v_mfma_f32_16x16x32_bf16 v[60:63], v[140:143], v[180:183], v[60:63]
	v_mfma_f32_16x16x32_bf16 v[48:51], v[132:135], v[194:197], v[48:51]
	v_mfma_f32_16x16x32_bf16 v[44:47], v[140:143], v[194:197], v[44:47]
	v_mfma_f32_16x16x32_bf16 v[30:33], v[132:135], v[228:231], v[30:33]
	v_mfma_f32_16x16x32_bf16 v[26:29], v[140:143], v[228:231], v[26:29]
	v_mfma_f32_16x16x32_bf16 v[14:17], v[132:135], v[242:245], v[14:17]
	v_mfma_f32_16x16x32_bf16 v[10:13], v[140:143], v[242:245], v[10:13]
	v_mfma_f32_16x16x32_bf16 v[64:67], v[136:139], v[184:187], v[64:67]
	v_mfma_f32_16x16x32_bf16 v[60:63], v[144:147], v[184:187], v[60:63]
	v_mfma_f32_16x16x32_bf16 v[48:51], v[136:139], v[224:227], v[48:51]
	v_mfma_f32_16x16x32_bf16 v[44:47], v[144:147], v[224:227], v[44:47]
	v_mfma_f32_16x16x32_bf16 v[30:33], v[136:139], v[238:241], v[30:33]
	v_mfma_f32_16x16x32_bf16 v[26:29], v[144:147], v[238:241], v[26:29]
	v_mfma_f32_16x16x32_bf16 v[14:17], v[136:139], v[246:249], v[14:17]
	v_mfma_f32_16x16x32_bf16 v[10:13], v[144:147], v[246:249], v[10:13]
	v_mfma_f32_16x16x32_bf16 v[56:59], v[148:151], v[180:183], v[56:59]
	v_mfma_f32_16x16x32_bf16 v[52:55], v[156:159], v[180:183], v[52:55]
	v_mfma_f32_16x16x32_bf16 v[40:43], v[148:151], v[194:197], v[40:43]
	v_mfma_f32_16x16x32_bf16 v[36:39], v[156:159], v[194:197], v[36:39]
	v_mfma_f32_16x16x32_bf16 v[22:25], v[148:151], v[228:231], v[22:25]
	v_mfma_f32_16x16x32_bf16 v[18:21], v[156:159], v[228:231], v[18:21]
	v_mfma_f32_16x16x32_bf16 v[6:9], v[148:151], v[242:245], v[6:9]
	v_mfma_f32_16x16x32_bf16 v[2:5], v[156:159], v[242:245], v[2:5]
	v_mfma_f32_16x16x32_bf16 v[56:59], v[152:155], v[184:187], v[56:59]
	v_mfma_f32_16x16x32_bf16 v[52:55], v[160:163], v[184:187], v[52:55]
	v_mfma_f32_16x16x32_bf16 v[40:43], v[152:155], v[224:227], v[40:43]
	v_mfma_f32_16x16x32_bf16 v[36:39], v[160:163], v[224:227], v[36:39]
	v_mfma_f32_16x16x32_bf16 v[22:25], v[152:155], v[238:241], v[22:25]
	v_mfma_f32_16x16x32_bf16 v[18:21], v[160:163], v[238:241], v[18:21]
	v_mfma_f32_16x16x32_bf16 v[6:9], v[152:155], v[246:249], v[6:9]
	v_mfma_f32_16x16x32_bf16 v[2:5], v[160:163], v[246:249], v[2:5]
	s_setprio 0
	s_barrier
	s_add_i32 s57, s57, 2
	s_add_u32 s23, s23, 0x100
	s_addc_u32 s25, s25, 0
	s_add_u32 s30, s30, 0x100
	s_addc_u32 s31, s31, 0
	s_cmp_gt_u32 s57, 13
	s_cbranch_scc0 .LBB0_673
	s_and_b64 vcc, exec, s[20:21]
	s_cbranch_vccz .LBB0_676
	s_barrier

.LBB0_787:
	s_add_u32 s4, s38, 0x80
	s_addc_u32 s5, s39, 0
	s_add_i32 s69, 0, 0x10000
	s_cmp_eq_u32 s68, 28
	s_cselect_b32 s5, s35, s5
	s_cselect_b32 s4, s34, s4
	s_cselect_b32 s45, s37, s31
	s_cselect_b32 s44, s36, s29
	s_add_i32 s74, 0, 0x14000
	v_add_u32_e32 v154, s69, v162
	v_add_u32_e32 v165, s74, v162
	ds_read_b128 v[132:135], v154
	ds_read_b128 v[136:139], v154 offset:1024
	ds_read_b128 v[140:143], v154 offset:2048
	ds_read_b128 v[154:157], v154 offset:3072
	ds_read_b128 v[158:161], v165
	ds_read_b128 v[166:169], v165 offset:1024
	ds_read_b128 v[170:173], v165 offset:2048
	ds_read_b128 v[174:177], v165 offset:3072
	v_lshl_add_u64 v[198:199], s[38:39], 0, v[152:153]
	s_add_i32 m0, s50, 0xc000
	ds_read_b128 v[178:181], v164
	ds_read_b128 v[182:185], v164 offset:1024
	ds_read_b128 v[186:189], v164 offset:2048
	ds_read_b128 v[190:193], v164 offset:3072
	ds_read_b128 v[194:197], v164 offset:4096
	ds_read_b128 v[224:227], v164 offset:5120
	ds_read_b128 v[228:231], v164 offset:6144
	ds_read_b128 v[238:241], v164 offset:7168
	global_load_lds_dwordx4 v[198:199], off
	v_lshl_add_u64 v[198:199], s[38:39], 0, v[150:151]
	s_add_i32 m0, s50, 0xe000
	s_nop 0
	global_load_lds_dwordx4 v[198:199], off
	s_waitcnt vmcnt(8)
	s_waitcnt lgkmcnt(0)
	s_barrier
	s_setprio 1
	s_waitcnt lgkmcnt(0)
	v_mfma_f32_16x16x32_bf16 v[128:131], v[132:135], v[178:181], v[128:131]
	v_mfma_f32_16x16x32_bf16 v[124:127], v[140:143], v[178:181], v[124:127]
	v_mfma_f32_16x16x32_bf16 v[120:123], v[132:135], v[186:189], v[120:123]
	v_mfma_f32_16x16x32_bf16 v[108:111], v[140:143], v[186:189], v[108:111]
	v_mfma_f32_16x16x32_bf16 v[104:107], v[132:135], v[194:197], v[104:107]
	v_mfma_f32_16x16x32_bf16 v[92:95], v[140:143], v[194:197], v[92:95]
	v_mfma_f32_16x16x32_bf16 v[88:91], v[132:135], v[228:231], v[88:91]
	v_mfma_f32_16x16x32_bf16 v[76:79], v[140:143], v[228:231], v[76:79]
	v_mfma_f32_16x16x32_bf16 v[128:131], v[136:139], v[182:185], v[128:131]
	v_mfma_f32_16x16x32_bf16 v[124:127], v[154:157], v[182:185], v[124:127]
	v_mfma_f32_16x16x32_bf16 v[120:123], v[136:139], v[190:193], v[120:123]
	v_mfma_f32_16x16x32_bf16 v[108:111], v[154:157], v[190:193], v[108:111]
	v_mfma_f32_16x16x32_bf16 v[104:107], v[136:139], v[224:227], v[104:107]
	v_mfma_f32_16x16x32_bf16 v[92:95], v[154:157], v[224:227], v[92:95]
	v_mfma_f32_16x16x32_bf16 v[88:91], v[136:139], v[238:241], v[88:91]
	v_mfma_f32_16x16x32_bf16 v[76:79], v[154:157], v[238:241], v[76:79]
	v_mfma_f32_16x16x32_bf16 v[116:119], v[158:161], v[178:181], v[116:119]
	v_mfma_f32_16x16x32_bf16 v[112:115], v[170:173], v[178:181], v[112:115]
	v_mfma_f32_16x16x32_bf16 v[100:103], v[158:161], v[186:189], v[100:103]
	v_mfma_f32_16x16x32_bf16 v[96:99], v[170:173], v[186:189], v[96:99]
	v_mfma_f32_16x16x32_bf16 v[84:87], v[158:161], v[194:197], v[84:87]
	v_mfma_f32_16x16x32_bf16 v[80:83], v[170:173], v[194:197], v[80:83]
	v_mfma_f32_16x16x32_bf16 v[72:75], v[158:161], v[228:231], v[72:75]
	v_mfma_f32_16x16x32_bf16 v[68:71], v[170:173], v[228:231], v[68:71]
	v_mfma_f32_16x16x32_bf16 v[116:119], v[166:169], v[182:185], v[116:119]
	v_mfma_f32_16x16x32_bf16 v[112:115], v[174:177], v[182:185], v[112:115]
	v_mfma_f32_16x16x32_bf16 v[100:103], v[166:169], v[190:193], v[100:103]
	v_mfma_f32_16x16x32_bf16 v[96:99], v[174:177], v[190:193], v[96:99]
	v_mfma_f32_16x16x32_bf16 v[84:87], v[166:169], v[224:227], v[84:87]
	v_mfma_f32_16x16x32_bf16 v[80:83], v[174:177], v[224:227], v[80:83]
	v_mfma_f32_16x16x32_bf16 v[72:75], v[166:169], v[238:241], v[72:75]
	v_mfma_f32_16x16x32_bf16 v[68:71], v[174:177], v[238:241], v[68:71]
	s_setprio 0
	s_barrier
	s_add_i32 s69, s69, s49
	v_lshl_add_u64 v[198:199], s[44:45], 0, v[34:35]
	s_mov_b32 m0, s69
	ds_read_b128 v[178:181], v164 offset:16384
	ds_read_b128 v[182:185], v164 offset:17408
	ds_read_b128 v[186:189], v164 offset:18432
	ds_read_b128 v[190:193], v164 offset:19456
	ds_read_b128 v[194:197], v164 offset:20480
	ds_read_b128 v[224:227], v164 offset:21504
	ds_read_b128 v[228:231], v164 offset:22528
	ds_read_b128 v[238:241], v164 offset:23552
	global_load_lds_dwordx4 v[198:199], off
	s_add_i32 m0, s69, 0x2000
	s_add_u32 s70, s44, 0x80000
	v_lshl_add_u64 v[212:213], s[44:45], 0, v[144:145]
	s_addc_u32 s71, s45, 0
	s_add_i32 s69, s74, s49
	global_load_lds_dwordx4 v[212:213], off
	v_lshl_add_u64 v[232:233], s[70:71], 0, v[34:35]
	s_mov_b32 m0, s69
	v_lshl_add_u64 v[242:243], s[4:5], 0, v[144:145]
	global_load_lds_dwordx4 v[232:233], off
	v_lshl_add_u64 v[232:233], s[70:71], 0, v[144:145]
	s_add_i32 m0, s69, 0x2000
	s_nop 0
	global_load_lds_dwordx4 v[232:233], off
	v_lshl_add_u64 v[232:233], s[4:5], 0, v[34:35]
	s_mov_b32 m0, s50
	s_nop 0
	global_load_lds_dwordx4 v[232:233], off
	s_mov_b32 m0, s51
	s_nop 0
	global_load_lds_dwordx4 v[242:243], off
	s_waitcnt vmcnt(8)
	s_waitcnt lgkmcnt(0)
	s_barrier
	s_setprio 1
	s_waitcnt lgkmcnt(0)
	v_mfma_f32_16x16x32_bf16 v[64:67], v[132:135], v[178:181], v[64:67]
	v_mfma_f32_16x16x32_bf16 v[60:63], v[140:143], v[178:181], v[60:63]
	v_mfma_f32_16x16x32_bf16 v[56:59], v[132:135], v[186:189], v[56:59]
	v_mfma_f32_16x16x32_bf16 v[44:47], v[140:143], v[186:189], v[44:47]
	v_mfma_f32_16x16x32_bf16 v[40:43], v[132:135], v[194:197], v[40:43]
	v_mfma_f32_16x16x32_bf16 v[26:29], v[140:143], v[194:197], v[26:29]
	v_mfma_f32_16x16x32_bf16 v[22:25], v[132:135], v[228:231], v[22:25]
	v_mfma_f32_16x16x32_bf16 v[10:13], v[140:143], v[228:231], v[10:13]
	v_mfma_f32_16x16x32_bf16 v[64:67], v[136:139], v[182:185], v[64:67]
	v_mfma_f32_16x16x32_bf16 v[60:63], v[154:157], v[182:185], v[60:63]
	v_mfma_f32_16x16x32_bf16 v[56:59], v[136:139], v[190:193], v[56:59]
	v_mfma_f32_16x16x32_bf16 v[44:47], v[154:157], v[190:193], v[44:47]
	v_mfma_f32_16x16x32_bf16 v[40:43], v[136:139], v[224:227], v[40:43]
	v_mfma_f32_16x16x32_bf16 v[26:29], v[154:157], v[224:227], v[26:29]
	v_mfma_f32_16x16x32_bf16 v[22:25], v[136:139], v[238:241], v[22:25]
	v_mfma_f32_16x16x32_bf16 v[10:13], v[154:157], v[238:241], v[10:13]
	v_mfma_f32_16x16x32_bf16 v[52:55], v[158:161], v[178:181], v[52:55]
	v_mfma_f32_16x16x32_bf16 v[48:51], v[170:173], v[178:181], v[48:51]
	v_mfma_f32_16x16x32_bf16 v[36:39], v[158:161], v[186:189], v[36:39]
	v_mfma_f32_16x16x32_bf16 v[30:33], v[170:173], v[186:189], v[30:33]
	v_mfma_f32_16x16x32_bf16 v[18:21], v[158:161], v[194:197], v[18:21]
	v_mfma_f32_16x16x32_bf16 v[14:17], v[170:173], v[194:197], v[14:17]
	v_mfma_f32_16x16x32_bf16 v[6:9], v[158:161], v[228:231], v[6:9]
	v_mfma_f32_16x16x32_bf16 v[2:5], v[170:173], v[228:231], v[2:5]
	v_mfma_f32_16x16x32_bf16 v[52:55], v[166:169], v[182:185], v[52:55]
	v_mfma_f32_16x16x32_bf16 v[48:51], v[174:177], v[182:185], v[48:51]
	v_mfma_f32_16x16x32_bf16 v[36:39], v[166:169], v[190:193], v[36:39]
	v_mfma_f32_16x16x32_bf16 v[30:33], v[174:177], v[190:193], v[30:33]
	v_mfma_f32_16x16x32_bf16 v[18:21], v[166:169], v[224:227], v[18:21]
	v_mfma_f32_16x16x32_bf16 v[14:17], v[174:177], v[224:227], v[14:17]
	v_mfma_f32_16x16x32_bf16 v[6:9], v[166:169], v[238:241], v[6:9]
	v_mfma_f32_16x16x32_bf16 v[2:5], v[174:177], v[238:241], v[2:5]
	s_setprio 0
	s_barrier
	s_add_i32 s69, 0, 0x18000
	s_add_i32 s70, 0, 0x1c000
	v_add_u32_e32 v154, s69, v162
	v_add_u32_e32 v165, s70, v162
	ds_read_b128 v[132:135], v154
	ds_read_b128 v[136:139], v154 offset:1024
	ds_read_b128 v[140:143], v154 offset:2048
	ds_read_b128 v[154:157], v154 offset:3072
	ds_read_b128 v[158:161], v165
	ds_read_b128 v[166:169], v165 offset:1024
	ds_read_b128 v[170:173], v165 offset:2048
	ds_read_b128 v[174:177], v165 offset:3072
	s_mov_b32 m0, s52
	v_lshl_add_u64 v[244:245], s[4:5], 0, v[148:149]
	ds_read_b128 v[178:181], v164 offset:32768
	ds_read_b128 v[182:185], v164 offset:33792
	ds_read_b128 v[186:189], v164 offset:34816
	ds_read_b128 v[190:193], v164 offset:35840
	ds_read_b128 v[194:197], v164 offset:36864
	ds_read_b128 v[224:227], v164 offset:37888
	ds_read_b128 v[228:231], v164 offset:38912
	ds_read_b128 v[238:241], v164 offset:39936
	global_load_lds_dwordx4 v[244:245], off
	v_lshl_add_u64 v[244:245], s[4:5], 0, v[146:147]
	s_mov_b32 m0, s53
	s_nop 0
	global_load_lds_dwordx4 v[244:245], off
	s_waitcnt vmcnt(8)
	s_waitcnt lgkmcnt(0)
	s_barrier
	s_setprio 1
	s_waitcnt lgkmcnt(0)
	v_mfma_f32_16x16x32_bf16 v[128:131], v[132:135], v[178:181], v[128:131]
	v_mfma_f32_16x16x32_bf16 v[124:127], v[140:143], v[178:181], v[124:127]
	v_mfma_f32_16x16x32_bf16 v[120:123], v[132:135], v[186:189], v[120:123]
	v_mfma_f32_16x16x32_bf16 v[108:111], v[140:143], v[186:189], v[108:111]
	v_mfma_f32_16x16x32_bf16 v[104:107], v[132:135], v[194:197], v[104:107]
	v_mfma_f32_16x16x32_bf16 v[92:95], v[140:143], v[194:197], v[92:95]
	v_mfma_f32_16x16x32_bf16 v[88:91], v[132:135], v[228:231], v[88:91]
	v_mfma_f32_16x16x32_bf16 v[76:79], v[140:143], v[228:231], v[76:79]
	v_mfma_f32_16x16x32_bf16 v[128:131], v[136:139], v[182:185], v[128:131]
	v_mfma_f32_16x16x32_bf16 v[124:127], v[154:157], v[182:185], v[124:127]
	v_mfma_f32_16x16x32_bf16 v[120:123], v[136:139], v[190:193], v[120:123]
	v_mfma_f32_16x16x32_bf16 v[108:111], v[154:157], v[190:193], v[108:111]
	v_mfma_f32_16x16x32_bf16 v[104:107], v[136:139], v[224:227], v[104:107]
	v_mfma_f32_16x16x32_bf16 v[92:95], v[154:157], v[224:227], v[92:95]
	v_mfma_f32_16x16x32_bf16 v[88:91], v[136:139], v[238:241], v[88:91]
	v_mfma_f32_16x16x32_bf16 v[76:79], v[154:157], v[238:241], v[76:79]
	v_mfma_f32_16x16x32_bf16 v[116:119], v[158:161], v[178:181], v[116:119]
	v_mfma_f32_16x16x32_bf16 v[112:115], v[170:173], v[178:181], v[112:115]
	v_mfma_f32_16x16x32_bf16 v[100:103], v[158:161], v[186:189], v[100:103]
	v_mfma_f32_16x16x32_bf16 v[96:99], v[170:173], v[186:189], v[96:99]
	v_mfma_f32_16x16x32_bf16 v[84:87], v[158:161], v[194:197], v[84:87]
	v_mfma_f32_16x16x32_bf16 v[80:83], v[170:173], v[194:197], v[80:83]
	v_mfma_f32_16x16x32_bf16 v[72:75], v[158:161], v[228:231], v[72:75]
	v_mfma_f32_16x16x32_bf16 v[68:71], v[170:173], v[228:231], v[68:71]
	v_mfma_f32_16x16x32_bf16 v[116:119], v[166:169], v[182:185], v[116:119]
	v_mfma_f32_16x16x32_bf16 v[112:115], v[174:177], v[182:185], v[112:115]
	v_mfma_f32_16x16x32_bf16 v[100:103], v[166:169], v[190:193], v[100:103]
	v_mfma_f32_16x16x32_bf16 v[96:99], v[174:177], v[190:193], v[96:99]
	v_mfma_f32_16x16x32_bf16 v[84:87], v[166:169], v[224:227], v[84:87]
	v_mfma_f32_16x16x32_bf16 v[80:83], v[174:177], v[224:227], v[80:83]
	v_mfma_f32_16x16x32_bf16 v[72:75], v[166:169], v[238:241], v[72:75]
	v_mfma_f32_16x16x32_bf16 v[68:71], v[174:177], v[238:241], v[68:71]
	s_setprio 0
	s_barrier
	s_add_i32 s4, s69, s49
	v_lshl_add_u64 v[198:199], v[198:199], 0, s[78:79]
	s_mov_b32 m0, s4
	ds_read_b128 v[178:181], v164 offset:49152
	ds_read_b128 v[182:185], v164 offset:50176
	ds_read_b128 v[186:189], v164 offset:51200
	ds_read_b128 v[190:193], v164 offset:52224
	ds_read_b128 v[194:197], v164 offset:53248
	ds_read_b128 v[224:227], v164 offset:54272
	ds_read_b128 v[228:231], v164 offset:55296
	ds_read_b128 v[238:241], v164 offset:56320
	global_load_lds_dwordx4 v[198:199], off
	s_add_i32 m0, s4, 0x2000
	s_add_u32 s4, s44, 0x80080
	v_lshl_add_u64 v[198:199], v[212:213], 0, s[78:79]
	s_addc_u32 s5, s45, 0
	s_add_i32 s44, s70, s49
	global_load_lds_dwordx4 v[198:199], off
	v_lshl_add_u64 v[198:199], s[4:5], 0, v[34:35]
	s_mov_b32 m0, s44
	s_nop 0
	global_load_lds_dwordx4 v[198:199], off
	v_lshl_add_u64 v[198:199], s[4:5], 0, v[144:145]
	s_add_i32 m0, s44, 0x2000
	s_nop 0
	global_load_lds_dwordx4 v[198:199], off
	v_lshl_add_u64 v[198:199], v[232:233], 0, s[78:79]
	s_mov_b32 m0, s54
	s_nop 0
	global_load_lds_dwordx4 v[198:199], off
	v_lshl_add_u64 v[198:199], v[242:243], 0, s[78:79]
	s_mov_b32 m0, s55
	s_nop 0
	global_load_lds_dwordx4 v[198:199], off
	s_waitcnt vmcnt(8)
	s_waitcnt lgkmcnt(0)
	s_barrier
	s_setprio 1
	s_waitcnt lgkmcnt(0)
	v_mfma_f32_16x16x32_bf16 v[64:67], v[132:135], v[178:181], v[64:67]
	v_mfma_f32_16x16x32_bf16 v[60:63], v[140:143], v[178:181], v[60:63]
	v_mfma_f32_16x16x32_bf16 v[56:59], v[132:135], v[186:189], v[56:59]
	v_mfma_f32_16x16x32_bf16 v[44:47], v[140:143], v[186:189], v[44:47]
	v_mfma_f32_16x16x32_bf16 v[40:43], v[132:135], v[194:197], v[40:43]
	v_mfma_f32_16x16x32_bf16 v[26:29], v[140:143], v[194:197], v[26:29]
	v_mfma_f32_16x16x32_bf16 v[22:25], v[132:135], v[228:231], v[22:25]
	v_mfma_f32_16x16x32_bf16 v[10:13], v[140:143], v[228:231], v[10:13]
	v_mfma_f32_16x16x32_bf16 v[64:67], v[136:139], v[182:185], v[64:67]
	v_mfma_f32_16x16x32_bf16 v[60:63], v[154:157], v[182:185], v[60:63]
	v_mfma_f32_16x16x32_bf16 v[56:59], v[136:139], v[190:193], v[56:59]
	v_mfma_f32_16x16x32_bf16 v[44:47], v[154:157], v[190:193], v[44:47]
	v_mfma_f32_16x16x32_bf16 v[40:43], v[136:139], v[224:227], v[40:43]
	v_mfma_f32_16x16x32_bf16 v[26:29], v[154:157], v[224:227], v[26:29]
	v_mfma_f32_16x16x32_bf16 v[22:25], v[136:139], v[238:241], v[22:25]
	v_mfma_f32_16x16x32_bf16 v[10:13], v[154:157], v[238:241], v[10:13]
	v_mfma_f32_16x16x32_bf16 v[52:55], v[158:161], v[178:181], v[52:55]
	v_mfma_f32_16x16x32_bf16 v[48:51], v[170:173], v[178:181], v[48:51]
	v_mfma_f32_16x16x32_bf16 v[36:39], v[158:161], v[186:189], v[36:39]
	v_mfma_f32_16x16x32_bf16 v[30:33], v[170:173], v[186:189], v[30:33]
	v_mfma_f32_16x16x32_bf16 v[18:21], v[158:161], v[194:197], v[18:21]
	v_mfma_f32_16x16x32_bf16 v[14:17], v[170:173], v[194:197], v[14:17]
	v_mfma_f32_16x16x32_bf16 v[6:9], v[158:161], v[228:231], v[6:9]
	v_mfma_f32_16x16x32_bf16 v[2:5], v[170:173], v[228:231], v[2:5]
	v_mfma_f32_16x16x32_bf16 v[52:55], v[166:169], v[182:185], v[52:55]
	v_mfma_f32_16x16x32_bf16 v[48:51], v[174:177], v[182:185], v[48:51]
	v_mfma_f32_16x16x32_bf16 v[36:39], v[166:169], v[190:193], v[36:39]
	v_mfma_f32_16x16x32_bf16 v[30:33], v[174:177], v[190:193], v[30:33]
	v_mfma_f32_16x16x32_bf16 v[18:21], v[166:169], v[224:227], v[18:21]
	v_mfma_f32_16x16x32_bf16 v[14:17], v[174:177], v[224:227], v[14:17]
	v_mfma_f32_16x16x32_bf16 v[6:9], v[166:169], v[238:241], v[6:9]
	v_mfma_f32_16x16x32_bf16 v[2:5], v[174:177], v[238:241], v[2:5]
	s_setprio 0
	s_barrier
	s_add_i32 s68, s68, 2
	s_add_u32 s29, s29, 0x100
	s_addc_u32 s31, s31, 0
	s_add_u32 s38, s38, 0x100
	s_addc_u32 s39, s39, 0
	s_cmp_gt_u32 s68, 29
	s_cbranch_scc0 .LBB0_787
	s_and_b64 vcc, exec, s[26:27]
	s_cbranch_vccz .LBB0_790
	s_barrier

.LBB0_899:
	s_add_u32 s4, s36, 0x80
	s_addc_u32 s5, s37, 0
	s_add_i32 s68, 0, 0x10000
	v_add_u32_e32 v83, s68, v81
	ds_read_b128 v[84:87], v83
	ds_read_b128 v[88:91], v83 offset:1024
	ds_read_b128 v[92:95], v83 offset:2048
	ds_read_b128 v[96:99], v83 offset:3072
	s_cmp_eq_u32 s65, 28
	s_cselect_b32 s39, s31, s5
	s_cselect_b32 s38, s30, s4
	s_cselect_b32 s5, s35, s64
	s_cselect_b32 s4, s34, s29
	v_lshl_add_u64 v[132:133], s[36:37], 0, v[78:79]
	s_add_i32 m0, s45, 0xc000
	ds_read_b128 v[100:103], v82
	ds_read_b128 v[104:107], v82 offset:1024
	ds_read_b128 v[108:111], v82 offset:2048
	ds_read_b128 v[112:115], v82 offset:3072
	ds_read_b128 v[116:119], v82 offset:4096
	ds_read_b128 v[120:123], v82 offset:5120
	ds_read_b128 v[124:127], v82 offset:6144
	ds_read_b128 v[128:131], v82 offset:7168
	global_load_lds_dwordx4 v[132:133], off
	v_lshl_add_u64 v[132:133], s[36:37], 0, v[76:77]
	s_add_i32 m0, s45, 0xe000
	s_nop 0
	global_load_lds_dwordx4 v[132:133], off
	s_waitcnt vmcnt(8)
	s_waitcnt lgkmcnt(0)
	s_barrier
	s_setprio 1
	s_waitcnt lgkmcnt(0)
	v_mfma_f32_16x16x32_bf16 v[64:67], v[84:87], v[100:103], v[64:67]
	v_mfma_f32_16x16x32_bf16 v[60:63], v[92:95], v[100:103], v[60:63]
	v_mfma_f32_16x16x32_bf16 v[56:59], v[84:87], v[108:111], v[56:59]
	v_mfma_f32_16x16x32_bf16 v[52:55], v[92:95], v[108:111], v[52:55]
	v_mfma_f32_16x16x32_bf16 v[48:51], v[84:87], v[116:119], v[48:51]
	v_mfma_f32_16x16x32_bf16 v[44:47], v[92:95], v[116:119], v[44:47]
	v_mfma_f32_16x16x32_bf16 v[40:43], v[84:87], v[124:127], v[40:43]
	v_mfma_f32_16x16x32_bf16 v[36:39], v[92:95], v[124:127], v[36:39]
	v_mfma_f32_16x16x32_bf16 v[64:67], v[88:91], v[104:107], v[64:67]
	v_mfma_f32_16x16x32_bf16 v[60:63], v[96:99], v[104:107], v[60:63]
	v_mfma_f32_16x16x32_bf16 v[56:59], v[88:91], v[112:115], v[56:59]
	v_mfma_f32_16x16x32_bf16 v[52:55], v[96:99], v[112:115], v[52:55]
	v_mfma_f32_16x16x32_bf16 v[48:51], v[88:91], v[120:123], v[48:51]
	v_mfma_f32_16x16x32_bf16 v[44:47], v[96:99], v[120:123], v[44:47]
	v_mfma_f32_16x16x32_bf16 v[40:43], v[88:91], v[128:131], v[40:43]
	v_mfma_f32_16x16x32_bf16 v[36:39], v[96:99], v[128:131], v[36:39]
	s_setprio 0
	s_barrier
	s_add_i32 s68, s68, s44
	v_lshl_add_u64 v[132:133], s[4:5], 0, v[34:35]
	s_mov_b32 m0, s68
	ds_read_b128 v[100:103], v82 offset:16384
	ds_read_b128 v[104:107], v82 offset:17408
	ds_read_b128 v[108:111], v82 offset:18432
	ds_read_b128 v[112:115], v82 offset:19456
	ds_read_b128 v[116:119], v82 offset:20480
	ds_read_b128 v[120:123], v82 offset:21504
	ds_read_b128 v[124:127], v82 offset:22528
	ds_read_b128 v[128:131], v82 offset:23552
	global_load_lds_dwordx4 v[132:133], off
	s_add_i32 m0, s68, 0x2000
	s_add_u32 s68, s4, 0x80000
	v_lshl_add_u64 v[134:135], s[4:5], 0, v[68:69]
	s_addc_u32 s69, s5, 0
	global_load_lds_dwordx4 v[134:135], off
	v_lshl_add_u64 v[136:137], s[68:69], 0, v[34:35]
	s_mov_b32 m0, s46
	v_lshl_add_u64 v[138:139], s[38:39], 0, v[68:69]
	global_load_lds_dwordx4 v[136:137], off
	v_lshl_add_u64 v[136:137], s[68:69], 0, v[68:69]
	s_mov_b32 m0, s47
	s_nop 0
	global_load_lds_dwordx4 v[136:137], off
	v_lshl_add_u64 v[136:137], s[38:39], 0, v[34:35]
	s_mov_b32 m0, s45
	s_nop 0
	global_load_lds_dwordx4 v[136:137], off
	s_mov_b32 m0, s48
	s_nop 0
	global_load_lds_dwordx4 v[138:139], off
	s_waitcnt vmcnt(8)
	s_waitcnt lgkmcnt(0)
	s_barrier
	s_setprio 1
	s_waitcnt lgkmcnt(0)
	v_mfma_f32_16x16x32_bf16 v[30:33], v[84:87], v[100:103], v[30:33]
	v_mfma_f32_16x16x32_bf16 v[26:29], v[92:95], v[100:103], v[26:29]
	v_mfma_f32_16x16x32_bf16 v[22:25], v[84:87], v[108:111], v[22:25]
	v_mfma_f32_16x16x32_bf16 v[18:21], v[92:95], v[108:111], v[18:21]
	v_mfma_f32_16x16x32_bf16 v[14:17], v[84:87], v[116:119], v[14:17]
	v_mfma_f32_16x16x32_bf16 v[10:13], v[92:95], v[116:119], v[10:13]
	v_mfma_f32_16x16x32_bf16 v[6:9], v[84:87], v[124:127], v[6:9]
	v_mfma_f32_16x16x32_bf16 v[2:5], v[92:95], v[124:127], v[2:5]
	v_mfma_f32_16x16x32_bf16 v[30:33], v[88:91], v[104:107], v[30:33]
	v_mfma_f32_16x16x32_bf16 v[26:29], v[96:99], v[104:107], v[26:29]
	v_mfma_f32_16x16x32_bf16 v[22:25], v[88:91], v[112:115], v[22:25]
	v_mfma_f32_16x16x32_bf16 v[18:21], v[96:99], v[112:115], v[18:21]
	v_mfma_f32_16x16x32_bf16 v[14:17], v[88:91], v[120:123], v[14:17]
	v_mfma_f32_16x16x32_bf16 v[10:13], v[96:99], v[120:123], v[10:13]
	v_mfma_f32_16x16x32_bf16 v[6:9], v[88:91], v[128:131], v[6:9]
	v_mfma_f32_16x16x32_bf16 v[2:5], v[96:99], v[128:131], v[2:5]
	s_setprio 0
	s_barrier
	s_add_i32 s68, 0, 0x18000
	v_add_u32_e32 v83, s68, v81
	ds_read_b128 v[84:87], v83
	ds_read_b128 v[88:91], v83 offset:1024
	ds_read_b128 v[92:95], v83 offset:2048
	ds_read_b128 v[96:99], v83 offset:3072
	s_mov_b32 m0, s49
	v_lshl_add_u64 v[140:141], s[38:39], 0, v[72:73]
	ds_read_b128 v[100:103], v82 offset:32768
	ds_read_b128 v[104:107], v82 offset:33792
	ds_read_b128 v[108:111], v82 offset:34816
	ds_read_b128 v[112:115], v82 offset:35840
	ds_read_b128 v[116:119], v82 offset:36864
	ds_read_b128 v[120:123], v82 offset:37888
	ds_read_b128 v[124:127], v82 offset:38912
	ds_read_b128 v[128:131], v82 offset:39936
	global_load_lds_dwordx4 v[140:141], off
	v_lshl_add_u64 v[140:141], s[38:39], 0, v[70:71]
	s_mov_b32 m0, s50
	s_nop 0
	global_load_lds_dwordx4 v[140:141], off
	s_waitcnt vmcnt(8)
	s_waitcnt lgkmcnt(0)
	s_barrier
	s_setprio 1
	s_waitcnt lgkmcnt(0)
	v_mfma_f32_16x16x32_bf16 v[64:67], v[84:87], v[100:103], v[64:67]
	v_mfma_f32_16x16x32_bf16 v[60:63], v[92:95], v[100:103], v[60:63]
	v_mfma_f32_16x16x32_bf16 v[56:59], v[84:87], v[108:111], v[56:59]
	v_mfma_f32_16x16x32_bf16 v[52:55], v[92:95], v[108:111], v[52:55]
	v_mfma_f32_16x16x32_bf16 v[48:51], v[84:87], v[116:119], v[48:51]
	v_mfma_f32_16x16x32_bf16 v[44:47], v[92:95], v[116:119], v[44:47]
	v_mfma_f32_16x16x32_bf16 v[40:43], v[84:87], v[124:127], v[40:43]
	v_mfma_f32_16x16x32_bf16 v[36:39], v[92:95], v[124:127], v[36:39]
	v_mfma_f32_16x16x32_bf16 v[64:67], v[88:91], v[104:107], v[64:67]
	v_mfma_f32_16x16x32_bf16 v[60:63], v[96:99], v[104:107], v[60:63]
	v_mfma_f32_16x16x32_bf16 v[56:59], v[88:91], v[112:115], v[56:59]
	v_mfma_f32_16x16x32_bf16 v[52:55], v[96:99], v[112:115], v[52:55]
	v_mfma_f32_16x16x32_bf16 v[48:51], v[88:91], v[120:123], v[48:51]
	v_mfma_f32_16x16x32_bf16 v[44:47], v[96:99], v[120:123], v[44:47]
	v_mfma_f32_16x16x32_bf16 v[40:43], v[88:91], v[128:131], v[40:43]
	v_mfma_f32_16x16x32_bf16 v[36:39], v[96:99], v[128:131], v[36:39]
	s_setprio 0
	s_barrier
	s_add_i32 s38, s68, s44
	v_lshl_add_u64 v[132:133], v[132:133], 0, s[78:79]
	s_mov_b32 m0, s38
	ds_read_b128 v[100:103], v82 offset:49152
	ds_read_b128 v[104:107], v82 offset:50176
	ds_read_b128 v[108:111], v82 offset:51200
	ds_read_b128 v[112:115], v82 offset:52224
	ds_read_b128 v[116:119], v82 offset:53248
	ds_read_b128 v[120:123], v82 offset:54272
	ds_read_b128 v[124:127], v82 offset:55296
	ds_read_b128 v[128:131], v82 offset:56320
	global_load_lds_dwordx4 v[132:133], off
	s_add_i32 m0, s38, 0x2000
	s_add_u32 s4, s4, 0x80080
	v_lshl_add_u64 v[132:133], v[134:135], 0, s[78:79]
	s_addc_u32 s5, s5, 0
	global_load_lds_dwordx4 v[132:133], off
	v_lshl_add_u64 v[132:133], s[4:5], 0, v[34:35]
	s_mov_b32 m0, s53
	s_nop 0
	global_load_lds_dwordx4 v[132:133], off
	v_lshl_add_u64 v[132:133], s[4:5], 0, v[68:69]
	s_mov_b32 m0, s54
	s_nop 0
	global_load_lds_dwordx4 v[132:133], off
	v_lshl_add_u64 v[132:133], v[136:137], 0, s[78:79]
	s_mov_b32 m0, s51
	s_nop 0
	global_load_lds_dwordx4 v[132:133], off
	v_lshl_add_u64 v[132:133], v[138:139], 0, s[78:79]
	s_mov_b32 m0, s52
	s_nop 0
	global_load_lds_dwordx4 v[132:133], off
	s_waitcnt vmcnt(8)
	s_waitcnt lgkmcnt(0)
	s_barrier
	s_setprio 1
	s_waitcnt lgkmcnt(0)
	v_mfma_f32_16x16x32_bf16 v[30:33], v[84:87], v[100:103], v[30:33]
	v_mfma_f32_16x16x32_bf16 v[26:29], v[92:95], v[100:103], v[26:29]
	v_mfma_f32_16x16x32_bf16 v[22:25], v[84:87], v[108:111], v[22:25]
	v_mfma_f32_16x16x32_bf16 v[18:21], v[92:95], v[108:111], v[18:21]
	v_mfma_f32_16x16x32_bf16 v[14:17], v[84:87], v[116:119], v[14:17]
	v_mfma_f32_16x16x32_bf16 v[10:13], v[92:95], v[116:119], v[10:13]
	v_mfma_f32_16x16x32_bf16 v[6:9], v[84:87], v[124:127], v[6:9]
	v_mfma_f32_16x16x32_bf16 v[2:5], v[92:95], v[124:127], v[2:5]
	v_mfma_f32_16x16x32_bf16 v[30:33], v[88:91], v[104:107], v[30:33]
	v_mfma_f32_16x16x32_bf16 v[26:29], v[96:99], v[104:107], v[26:29]
	v_mfma_f32_16x16x32_bf16 v[22:25], v[88:91], v[112:115], v[22:25]
	v_mfma_f32_16x16x32_bf16 v[18:21], v[96:99], v[112:115], v[18:21]
	v_mfma_f32_16x16x32_bf16 v[14:17], v[88:91], v[120:123], v[14:17]
	v_mfma_f32_16x16x32_bf16 v[10:13], v[96:99], v[120:123], v[10:13]
	v_mfma_f32_16x16x32_bf16 v[6:9], v[88:91], v[128:131], v[6:9]
	v_mfma_f32_16x16x32_bf16 v[2:5], v[96:99], v[128:131], v[2:5]
	s_setprio 0
	s_barrier
	s_add_i32 s65, s65, 2
	s_add_u32 s29, s29, 0x100
	s_addc_u32 s64, s64, 0
	s_add_u32 s36, s36, 0x100
	s_addc_u32 s37, s37, 0
	s_cmp_gt_u32 s65, 29
	s_cbranch_scc0 .LBB0_899
	s_and_b64 vcc, exec, s[24:25]
	s_cbranch_vccz .LBB0_903
	s_barrier
	s_andn2_b64 vcc, exec, s[26:27]
	s_cbranch_vccz .LBB0_904

.LBB0_1096:
	s_add_u32 s14, s40, 0x80
	s_addc_u32 s15, s41, 0
	s_and_b64 s[4:5], s[4:5], exec
	s_cselect_b32 s5, s35, s71
	s_cselect_b32 s4, s34, s70
	s_mov_b32 m0, s49
	s_cselect_b32 s15, s39, s15
	s_cselect_b32 s14, s38, s14
	v_lshl_add_u64 v[198:199], s[4:5], 0, v[168:169]
	s_add_u32 s74, s4, 0x80000
	ds_read_b128 v[186:189], v182 offset:16384
	ds_read_b128 v[190:193], v182 offset:17408
	ds_read_b128 v[194:197], v182 offset:18432
	ds_read_b128 v[224:227], v182 offset:19456
	ds_read_b128 v[228:231], v182 offset:20480
	ds_read_b128 v[238:241], v182 offset:21504
	ds_read_b128 v[242:245], v182 offset:22528
	ds_read_b128 v[246:249], v182 offset:23552
	global_load_lds_dwordx4 v[198:199], off
	v_lshl_add_u64 v[212:213], s[4:5], 0, v[166:167]
	s_mov_b32 m0, s50
	s_addc_u32 s75, s5, 0
	global_load_lds_dwordx4 v[212:213], off
	v_lshl_add_u64 v[232:233], s[74:75], 0, v[168:169]
	s_mov_b32 m0, s51
	v_mov_b32_e32 v171, v35
	global_load_lds_dwordx4 v[232:233], off
	v_lshl_add_u64 v[232:233], s[74:75], 0, v[166:167]
	s_mov_b32 m0, s52
	v_mov_b32_e32 v173, v35
	global_load_lds_dwordx4 v[232:233], off
	s_mov_b32 m0, s48
	v_mov_b32_e32 v175, v35
	global_load_lds_dwordx4 v34, s[14:15]
	s_mov_b32 m0, s53
	v_lshl_add_u64 v[232:233], s[14:15], 0, v[34:35]
	global_load_lds_dwordx4 v170, s[14:15]
	s_waitcnt vmcnt(8)
	s_waitcnt lgkmcnt(0)
	v_lshl_add_u64 v[250:251], s[14:15], 0, v[170:171]
	s_barrier
	s_setprio 1
	s_waitcnt lgkmcnt(0)
	v_mfma_f32_16x16x32_bf16 v[64:67], v[148:151], v[186:189], v[64:67]
	v_mfma_f32_16x16x32_bf16 v[60:63], v[156:159], v[186:189], v[60:63]
	v_mfma_f32_16x16x32_bf16 v[48:51], v[148:151], v[194:197], v[48:51]
	v_mfma_f32_16x16x32_bf16 v[44:47], v[156:159], v[194:197], v[44:47]
	v_mfma_f32_16x16x32_bf16 v[30:33], v[148:151], v[228:231], v[30:33]
	v_mfma_f32_16x16x32_bf16 v[26:29], v[156:159], v[228:231], v[26:29]
	v_mfma_f32_16x16x32_bf16 v[14:17], v[148:151], v[242:245], v[14:17]
	v_mfma_f32_16x16x32_bf16 v[10:13], v[156:159], v[242:245], v[10:13]
	v_mfma_f32_16x16x32_bf16 v[64:67], v[152:155], v[190:193], v[64:67]
	v_mfma_f32_16x16x32_bf16 v[60:63], v[160:163], v[190:193], v[60:63]
	v_mfma_f32_16x16x32_bf16 v[48:51], v[152:155], v[224:227], v[48:51]
	v_mfma_f32_16x16x32_bf16 v[44:47], v[160:163], v[224:227], v[44:47]
	v_mfma_f32_16x16x32_bf16 v[30:33], v[152:155], v[238:241], v[30:33]
	v_mfma_f32_16x16x32_bf16 v[26:29], v[160:163], v[238:241], v[26:29]
	v_mfma_f32_16x16x32_bf16 v[14:17], v[152:155], v[246:249], v[14:17]
	v_mfma_f32_16x16x32_bf16 v[10:13], v[160:163], v[246:249], v[10:13]
	v_mfma_f32_16x16x32_bf16 v[56:59], v[132:135], v[186:189], v[56:59]
	v_mfma_f32_16x16x32_bf16 v[52:55], v[140:143], v[186:189], v[52:55]
	v_mfma_f32_16x16x32_bf16 v[40:43], v[132:135], v[194:197], v[40:43]
	v_mfma_f32_16x16x32_bf16 v[36:39], v[140:143], v[194:197], v[36:39]
	v_mfma_f32_16x16x32_bf16 v[22:25], v[132:135], v[228:231], v[22:25]
	v_mfma_f32_16x16x32_bf16 v[18:21], v[140:143], v[228:231], v[18:21]
	v_mfma_f32_16x16x32_bf16 v[6:9], v[132:135], v[242:245], v[6:9]
	v_mfma_f32_16x16x32_bf16 v[2:5], v[140:143], v[242:245], v[2:5]
	v_mfma_f32_16x16x32_bf16 v[56:59], v[136:139], v[190:193], v[56:59]
	v_mfma_f32_16x16x32_bf16 v[52:55], v[144:147], v[190:193], v[52:55]
	v_mfma_f32_16x16x32_bf16 v[40:43], v[136:139], v[224:227], v[40:43]
	v_mfma_f32_16x16x32_bf16 v[36:39], v[144:147], v[224:227], v[36:39]
	v_mfma_f32_16x16x32_bf16 v[22:25], v[136:139], v[238:241], v[22:25]
	v_mfma_f32_16x16x32_bf16 v[18:21], v[144:147], v[238:241], v[18:21]
	v_mfma_f32_16x16x32_bf16 v[6:9], v[136:139], v[246:249], v[6:9]
	v_mfma_f32_16x16x32_bf16 v[2:5], v[144:147], v[246:249], v[2:5]
	s_setprio 0
	s_barrier
	s_add_i32 s43, 0, 0x18000
	s_add_i32 s74, 0, 0x1c000
	v_add_u32_e32 v144, s43, v180
	v_add_u32_e32 v160, s74, v180
	ds_read_b128 v[132:135], v144
	ds_read_b128 v[136:139], v144 offset:1024
	ds_read_b128 v[140:143], v144 offset:2048
	ds_read_b128 v[144:147], v144 offset:3072
	ds_read_b128 v[148:151], v160
	ds_read_b128 v[152:155], v160 offset:1024
	ds_read_b128 v[156:159], v160 offset:2048
	ds_read_b128 v[160:163], v160 offset:3072
	s_mov_b32 m0, s54
	v_lshl_add_u64 v[208:209], s[14:15], 0, v[172:173]
	ds_read_b128 v[186:189], v182 offset:32768
	ds_read_b128 v[190:193], v182 offset:33792
	ds_read_b128 v[194:197], v182 offset:34816
	ds_read_b128 v[224:227], v182 offset:35840
	ds_read_b128 v[228:231], v182 offset:36864
	ds_read_b128 v[238:241], v182 offset:37888
	ds_read_b128 v[242:245], v182 offset:38912
	ds_read_b128 v[246:249], v182 offset:39936
	global_load_lds_dwordx4 v[208:209], off
	v_lshl_add_u64 v[208:209], s[14:15], 0, v[174:175]
	s_mov_b32 m0, s55
	s_nop 0
	global_load_lds_dwordx4 v[208:209], off
	s_waitcnt vmcnt(8)
	s_waitcnt lgkmcnt(0)
	s_barrier
	s_setprio 1
	s_waitcnt lgkmcnt(0)
	v_mfma_f32_16x16x32_bf16 v[128:131], v[132:135], v[186:189], v[128:131]
	v_mfma_f32_16x16x32_bf16 v[124:127], v[140:143], v[186:189], v[124:127]
	v_mfma_f32_16x16x32_bf16 v[112:115], v[132:135], v[194:197], v[112:115]
	v_mfma_f32_16x16x32_bf16 v[108:111], v[140:143], v[194:197], v[108:111]
	v_mfma_f32_16x16x32_bf16 v[96:99], v[132:135], v[228:231], v[96:99]
	v_mfma_f32_16x16x32_bf16 v[92:95], v[140:143], v[228:231], v[92:95]
	v_mfma_f32_16x16x32_bf16 v[80:83], v[132:135], v[242:245], v[80:83]
	v_mfma_f32_16x16x32_bf16 v[76:79], v[140:143], v[242:245], v[76:79]
	v_mfma_f32_16x16x32_bf16 v[128:131], v[136:139], v[190:193], v[128:131]
	v_mfma_f32_16x16x32_bf16 v[124:127], v[144:147], v[190:193], v[124:127]
	v_mfma_f32_16x16x32_bf16 v[112:115], v[136:139], v[224:227], v[112:115]
	v_mfma_f32_16x16x32_bf16 v[108:111], v[144:147], v[224:227], v[108:111]
	v_mfma_f32_16x16x32_bf16 v[96:99], v[136:139], v[238:241], v[96:99]
	v_mfma_f32_16x16x32_bf16 v[92:95], v[144:147], v[238:241], v[92:95]
	v_mfma_f32_16x16x32_bf16 v[80:83], v[136:139], v[246:249], v[80:83]
	v_mfma_f32_16x16x32_bf16 v[76:79], v[144:147], v[246:249], v[76:79]
	v_mfma_f32_16x16x32_bf16 v[120:123], v[148:151], v[186:189], v[120:123]
	v_mfma_f32_16x16x32_bf16 v[116:119], v[156:159], v[186:189], v[116:119]
	v_mfma_f32_16x16x32_bf16 v[104:107], v[148:151], v[194:197], v[104:107]
	v_mfma_f32_16x16x32_bf16 v[100:103], v[156:159], v[194:197], v[100:103]
	v_mfma_f32_16x16x32_bf16 v[88:91], v[148:151], v[228:231], v[88:91]
	v_mfma_f32_16x16x32_bf16 v[84:87], v[156:159], v[228:231], v[84:87]
	v_mfma_f32_16x16x32_bf16 v[72:75], v[148:151], v[242:245], v[72:75]
	v_mfma_f32_16x16x32_bf16 v[68:71], v[156:159], v[242:245], v[68:71]
	v_mfma_f32_16x16x32_bf16 v[120:123], v[152:155], v[190:193], v[120:123]
	v_mfma_f32_16x16x32_bf16 v[116:119], v[160:163], v[190:193], v[116:119]
	v_mfma_f32_16x16x32_bf16 v[104:107], v[152:155], v[224:227], v[104:107]
	v_mfma_f32_16x16x32_bf16 v[100:103], v[160:163], v[224:227], v[100:103]
	v_mfma_f32_16x16x32_bf16 v[88:91], v[152:155], v[238:241], v[88:91]
	v_mfma_f32_16x16x32_bf16 v[84:87], v[160:163], v[238:241], v[84:87]
	v_mfma_f32_16x16x32_bf16 v[72:75], v[152:155], v[246:249], v[72:75]
	v_mfma_f32_16x16x32_bf16 v[68:71], v[160:163], v[246:249], v[68:71]
	s_setprio 0
	s_barrier
	s_add_i32 s14, s43, s21
	v_lshl_add_u64 v[198:199], v[198:199], 0, s[78:79]
	s_mov_b32 m0, s14
	ds_read_b128 v[186:189], v182 offset:49152
	ds_read_b128 v[190:193], v182 offset:50176
	ds_read_b128 v[194:197], v182 offset:51200
	ds_read_b128 v[224:227], v182 offset:52224
	ds_read_b128 v[228:231], v182 offset:53248
	ds_read_b128 v[238:241], v182 offset:54272
	ds_read_b128 v[242:245], v182 offset:55296
	ds_read_b128 v[246:249], v182 offset:56320
	global_load_lds_dwordx4 v[198:199], off
	s_add_i32 m0, s14, 0x2000
	s_add_u32 s4, s4, 0x80080
	v_lshl_add_u64 v[198:199], v[212:213], 0, s[78:79]
	s_addc_u32 s5, s5, 0
	s_add_i32 s14, s74, s21
	global_load_lds_dwordx4 v[198:199], off
	v_lshl_add_u64 v[198:199], s[4:5], 0, v[168:169]
	s_mov_b32 m0, s14
	s_nop 0
	global_load_lds_dwordx4 v[198:199], off
	v_lshl_add_u64 v[198:199], s[4:5], 0, v[166:167]
	s_add_i32 m0, s14, 0x2000
	s_nop 0
	global_load_lds_dwordx4 v[198:199], off
	v_lshl_add_u64 v[198:199], v[232:233], 0, s[78:79]
	s_mov_b32 m0, s56
	s_nop 0
	global_load_lds_dwordx4 v[198:199], off
	v_lshl_add_u64 v[198:199], v[250:251], 0, s[78:79]
	s_mov_b32 m0, s57
	s_nop 0
	global_load_lds_dwordx4 v[198:199], off
	s_waitcnt vmcnt(8)
	s_waitcnt lgkmcnt(0)
	s_barrier
	s_setprio 1
	s_waitcnt lgkmcnt(0)
	v_mfma_f32_16x16x32_bf16 v[64:67], v[132:135], v[186:189], v[64:67]
	v_mfma_f32_16x16x32_bf16 v[60:63], v[140:143], v[186:189], v[60:63]
	v_mfma_f32_16x16x32_bf16 v[48:51], v[132:135], v[194:197], v[48:51]
	v_mfma_f32_16x16x32_bf16 v[44:47], v[140:143], v[194:197], v[44:47]
	v_mfma_f32_16x16x32_bf16 v[30:33], v[132:135], v[228:231], v[30:33]
	v_mfma_f32_16x16x32_bf16 v[26:29], v[140:143], v[228:231], v[26:29]
	v_mfma_f32_16x16x32_bf16 v[14:17], v[132:135], v[242:245], v[14:17]
	v_mfma_f32_16x16x32_bf16 v[10:13], v[140:143], v[242:245], v[10:13]
	v_mfma_f32_16x16x32_bf16 v[64:67], v[136:139], v[190:193], v[64:67]
	v_mfma_f32_16x16x32_bf16 v[60:63], v[144:147], v[190:193], v[60:63]
	v_mfma_f32_16x16x32_bf16 v[48:51], v[136:139], v[224:227], v[48:51]
	v_mfma_f32_16x16x32_bf16 v[44:47], v[144:147], v[224:227], v[44:47]
	v_mfma_f32_16x16x32_bf16 v[30:33], v[136:139], v[238:241], v[30:33]
	v_mfma_f32_16x16x32_bf16 v[26:29], v[144:147], v[238:241], v[26:29]
	v_mfma_f32_16x16x32_bf16 v[14:17], v[136:139], v[246:249], v[14:17]
	v_mfma_f32_16x16x32_bf16 v[10:13], v[144:147], v[246:249], v[10:13]
	v_mfma_f32_16x16x32_bf16 v[56:59], v[148:151], v[186:189], v[56:59]
	v_mfma_f32_16x16x32_bf16 v[52:55], v[156:159], v[186:189], v[52:55]
	v_mfma_f32_16x16x32_bf16 v[40:43], v[148:151], v[194:197], v[40:43]
	v_mfma_f32_16x16x32_bf16 v[36:39], v[156:159], v[194:197], v[36:39]
	v_mfma_f32_16x16x32_bf16 v[22:25], v[148:151], v[228:231], v[22:25]
	v_mfma_f32_16x16x32_bf16 v[18:21], v[156:159], v[228:231], v[18:21]
	v_mfma_f32_16x16x32_bf16 v[6:9], v[148:151], v[242:245], v[6:9]
	v_mfma_f32_16x16x32_bf16 v[2:5], v[156:159], v[242:245], v[2:5]
	v_mfma_f32_16x16x32_bf16 v[56:59], v[152:155], v[190:193], v[56:59]
	v_mfma_f32_16x16x32_bf16 v[52:55], v[160:163], v[190:193], v[52:55]
	v_mfma_f32_16x16x32_bf16 v[40:43], v[152:155], v[224:227], v[40:43]
	v_mfma_f32_16x16x32_bf16 v[36:39], v[160:163], v[224:227], v[36:39]
	v_mfma_f32_16x16x32_bf16 v[22:25], v[152:155], v[238:241], v[22:25]
	v_mfma_f32_16x16x32_bf16 v[18:21], v[160:163], v[238:241], v[18:21]
	v_mfma_f32_16x16x32_bf16 v[6:9], v[152:155], v[246:249], v[6:9]
	v_mfma_f32_16x16x32_bf16 v[2:5], v[160:163], v[246:249], v[2:5]
	s_setprio 0
	s_barrier
	s_add_i32 s42, s42, 2
	s_add_u32 s70, s70, 0x100
	s_addc_u32 s71, s71, 0
	s_add_u32 s40, s40, 0x100
	s_addc_u32 s41, s41, 0
	s_cmp_gt_u32 s42, 29
	s_cbranch_scc1 .LBB0_1099
.LBB0_1097:
	v_add_u32_e32 v132, 0, v180
	v_add_u32_e32 v133, 0x10000, v132
	v_add_u32_e32 v144, 0x14000, v132
	ds_read_b128 v[148:151], v133
	ds_read_b128 v[152:155], v133 offset:1024
	ds_read_b128 v[156:159], v133 offset:2048
	ds_read_b128 v[160:163], v133 offset:3072
	ds_read_b128 v[132:135], v144
	ds_read_b128 v[136:139], v144 offset:1024
	ds_read_b128 v[140:143], v144 offset:2048
	ds_read_b128 v[144:147], v144 offset:3072
	s_cmp_eq_u32 s42, 28
	s_cselect_b64 s[4:5], -1, 0
	s_add_i32 m0, s48, 0xc000
	ds_read_b128 v[186:189], v182
	ds_read_b128 v[190:193], v182 offset:1024
	ds_read_b128 v[194:197], v182 offset:2048
	ds_read_b128 v[224:227], v182 offset:3072
	ds_read_b128 v[228:231], v182 offset:4096
	ds_read_b128 v[238:241], v182 offset:5120
	ds_read_b128 v[242:245], v182 offset:6144
	ds_read_b128 v[246:249], v182 offset:7168
	global_load_lds_dwordx4 v172, s[40:41]
	s_add_i32 m0, s48, 0xe000
	s_nop 0
	global_load_lds_dwordx4 v174, s[40:41]
	s_waitcnt vmcnt(8)
	s_waitcnt lgkmcnt(0)
	s_barrier
	s_setprio 1
	s_waitcnt lgkmcnt(0)
	v_mfma_f32_16x16x32_bf16 v[128:131], v[148:151], v[186:189], v[128:131]
	v_mfma_f32_16x16x32_bf16 v[124:127], v[156:159], v[186:189], v[124:127]
	v_mfma_f32_16x16x32_bf16 v[112:115], v[148:151], v[194:197], v[112:115]
	v_mfma_f32_16x16x32_bf16 v[108:111], v[156:159], v[194:197], v[108:111]
	v_mfma_f32_16x16x32_bf16 v[96:99], v[148:151], v[228:231], v[96:99]
	v_mfma_f32_16x16x32_bf16 v[92:95], v[156:159], v[228:231], v[92:95]
	v_mfma_f32_16x16x32_bf16 v[80:83], v[148:151], v[242:245], v[80:83]
	v_mfma_f32_16x16x32_bf16 v[76:79], v[156:159], v[242:245], v[76:79]
	v_mfma_f32_16x16x32_bf16 v[128:131], v[152:155], v[190:193], v[128:131]
	v_mfma_f32_16x16x32_bf16 v[124:127], v[160:163], v[190:193], v[124:127]
	v_mfma_f32_16x16x32_bf16 v[112:115], v[152:155], v[224:227], v[112:115]
	v_mfma_f32_16x16x32_bf16 v[108:111], v[160:163], v[224:227], v[108:111]
	v_mfma_f32_16x16x32_bf16 v[96:99], v[152:155], v[238:241], v[96:99]
	v_mfma_f32_16x16x32_bf16 v[92:95], v[160:163], v[238:241], v[92:95]
	v_mfma_f32_16x16x32_bf16 v[80:83], v[152:155], v[246:249], v[80:83]
	v_mfma_f32_16x16x32_bf16 v[76:79], v[160:163], v[246:249], v[76:79]
	v_mfma_f32_16x16x32_bf16 v[120:123], v[132:135], v[186:189], v[120:123]
	v_mfma_f32_16x16x32_bf16 v[116:119], v[140:143], v[186:189], v[116:119]
	v_mfma_f32_16x16x32_bf16 v[104:107], v[132:135], v[194:197], v[104:107]
	v_mfma_f32_16x16x32_bf16 v[100:103], v[140:143], v[194:197], v[100:103]
	v_mfma_f32_16x16x32_bf16 v[88:91], v[132:135], v[228:231], v[88:91]
	v_mfma_f32_16x16x32_bf16 v[84:87], v[140:143], v[228:231], v[84:87]
	v_mfma_f32_16x16x32_bf16 v[72:75], v[132:135], v[242:245], v[72:75]
	v_mfma_f32_16x16x32_bf16 v[68:71], v[140:143], v[242:245], v[68:71]
	v_mfma_f32_16x16x32_bf16 v[120:123], v[136:139], v[190:193], v[120:123]
	v_mfma_f32_16x16x32_bf16 v[116:119], v[144:147], v[190:193], v[116:119]
	v_mfma_f32_16x16x32_bf16 v[104:107], v[136:139], v[224:227], v[104:107]
	v_mfma_f32_16x16x32_bf16 v[100:103], v[144:147], v[224:227], v[100:103]
	v_mfma_f32_16x16x32_bf16 v[88:91], v[136:139], v[238:241], v[88:91]
	v_mfma_f32_16x16x32_bf16 v[84:87], v[144:147], v[238:241], v[84:87]
	v_mfma_f32_16x16x32_bf16 v[72:75], v[136:139], v[246:249], v[72:75]
	v_mfma_f32_16x16x32_bf16 v[68:71], v[144:147], v[246:249], v[68:71]
	s_setprio 0
	s_barrier
	s_and_b64 s[14:15], s[36:37], s[4:5]
	s_andn2_b64 vcc, exec, s[14:15]
	s_cbranch_vccnz .LBB0_1096
	ds_read2st64_b32 v[170:171], v183 offset1:2
	ds_read2st64_b32 v[172:173], v184 offset1:2
	s_waitcnt lgkmcnt(0)
	v_lshl_add_u32 v34, v170, 12, v176
	v_lshl_add_u32 v170, v172, 12, v178
	v_lshl_add_u32 v172, v171, 12, v176
	v_lshl_add_u32 v174, v173, 12, v178
	s_branch .LBB0_1096

.LBB0_1199:
	s_add_u32 s4, s34, 0x80
	s_addc_u32 s5, s35, 0
	s_add_i32 s53, 0, 0x10000
	s_cmp_eq_u32 s52, 4
	s_cselect_b32 s5, s27, s5
	s_cselect_b32 s4, s26, s4
	v_add_u32_e32 v34, s53, v1
	s_cselect_b32 s37, s29, s51
	s_cselect_b32 s36, s28, s50
	s_add_i32 s56, 0, 0x14000
	ds_read_b128 v[154:157], v34
	ds_read_b128 v[158:161], v34 offset:1024
	ds_read_b128 v[162:165], v34 offset:2048
	ds_read_b128 v[166:169], v34 offset:3072
	v_add_u32_e32 v34, s56, v1
	ds_read_b128 v[170:173], v34
	ds_read_b128 v[174:177], v34 offset:1024
	ds_read_b128 v[178:181], v34 offset:2048
	ds_read_b128 v[182:185], v34 offset:3072
	v_lshl_add_u64 v[148:149], s[34:35], 0, v[146:147]
	s_add_i32 m0, s41, 0xc000
	ds_read_b128 v[186:189], v152
	ds_read_b128 v[190:193], v152 offset:1024
	ds_read_b128 v[194:197], v152 offset:2048
	ds_read_b128 v[224:227], v152 offset:3072
	ds_read_b128 v[228:231], v152 offset:4096
	ds_read_b128 v[238:241], v152 offset:5120
	ds_read_b128 v[242:245], v152 offset:6144
	ds_read_b128 v[246:249], v152 offset:7168
	global_load_lds_dwordx4 v[148:149], off
	v_lshl_add_u64 v[148:149], s[34:35], 0, v[144:145]
	s_add_i32 m0, s41, 0xe000
	s_nop 0
	global_load_lds_dwordx4 v[148:149], off
	s_waitcnt vmcnt(8)
	s_waitcnt lgkmcnt(0)
	s_barrier
	s_setprio 1
	s_waitcnt lgkmcnt(0)
	v_mfma_f32_16x16x32_bf16 v[128:131], v[154:157], v[186:189], v[128:131]
	v_mfma_f32_16x16x32_bf16 v[124:127], v[162:165], v[186:189], v[124:127]
	v_mfma_f32_16x16x32_bf16 v[116:119], v[154:157], v[194:197], v[116:119]
	v_mfma_f32_16x16x32_bf16 v[108:111], v[162:165], v[194:197], v[108:111]
	v_mfma_f32_16x16x32_bf16 v[100:103], v[154:157], v[228:231], v[100:103]
	v_mfma_f32_16x16x32_bf16 v[92:95], v[162:165], v[228:231], v[92:95]
	v_mfma_f32_16x16x32_bf16 v[84:87], v[154:157], v[242:245], v[84:87]
	v_mfma_f32_16x16x32_bf16 v[76:79], v[162:165], v[242:245], v[76:79]
	v_mfma_f32_16x16x32_bf16 v[128:131], v[158:161], v[190:193], v[128:131]
	v_mfma_f32_16x16x32_bf16 v[124:127], v[166:169], v[190:193], v[124:127]
	v_mfma_f32_16x16x32_bf16 v[116:119], v[158:161], v[224:227], v[116:119]
	v_mfma_f32_16x16x32_bf16 v[108:111], v[166:169], v[224:227], v[108:111]
	v_mfma_f32_16x16x32_bf16 v[100:103], v[158:161], v[238:241], v[100:103]
	v_mfma_f32_16x16x32_bf16 v[92:95], v[166:169], v[238:241], v[92:95]
	v_mfma_f32_16x16x32_bf16 v[84:87], v[158:161], v[246:249], v[84:87]
	v_mfma_f32_16x16x32_bf16 v[76:79], v[166:169], v[246:249], v[76:79]
	v_mfma_f32_16x16x32_bf16 v[120:123], v[170:173], v[186:189], v[120:123]
	v_mfma_f32_16x16x32_bf16 v[112:115], v[178:181], v[186:189], v[112:115]
	v_mfma_f32_16x16x32_bf16 v[104:107], v[170:173], v[194:197], v[104:107]
	v_mfma_f32_16x16x32_bf16 v[96:99], v[178:181], v[194:197], v[96:99]
	v_mfma_f32_16x16x32_bf16 v[88:91], v[170:173], v[228:231], v[88:91]
	v_mfma_f32_16x16x32_bf16 v[80:83], v[178:181], v[228:231], v[80:83]
	v_mfma_f32_16x16x32_bf16 v[72:75], v[170:173], v[242:245], v[72:75]
	v_mfma_f32_16x16x32_bf16 v[68:71], v[178:181], v[242:245], v[68:71]
	v_mfma_f32_16x16x32_bf16 v[120:123], v[174:177], v[190:193], v[120:123]
	v_mfma_f32_16x16x32_bf16 v[112:115], v[182:185], v[190:193], v[112:115]
	v_mfma_f32_16x16x32_bf16 v[104:107], v[174:177], v[224:227], v[104:107]
	v_mfma_f32_16x16x32_bf16 v[96:99], v[182:185], v[224:227], v[96:99]
	v_mfma_f32_16x16x32_bf16 v[88:91], v[174:177], v[238:241], v[88:91]
	v_mfma_f32_16x16x32_bf16 v[80:83], v[182:185], v[238:241], v[80:83]
	v_mfma_f32_16x16x32_bf16 v[72:75], v[174:177], v[246:249], v[72:75]
	v_mfma_f32_16x16x32_bf16 v[68:71], v[182:185], v[246:249], v[68:71]
	s_setprio 0
	s_barrier
	s_add_i32 s53, s53, s14
	v_lshl_add_u64 v[148:149], s[36:37], 0, v[138:139]
	s_mov_b32 m0, s53
	ds_read_b128 v[186:189], v152 offset:16384
	ds_read_b128 v[190:193], v152 offset:17408
	ds_read_b128 v[194:197], v152 offset:18432
	ds_read_b128 v[224:227], v152 offset:19456
	ds_read_b128 v[228:231], v152 offset:20480
	ds_read_b128 v[238:241], v152 offset:21504
	ds_read_b128 v[242:245], v152 offset:22528
	ds_read_b128 v[246:249], v152 offset:23552
	global_load_lds_dwordx4 v[148:149], off
	s_add_i32 m0, s53, 0x2000
	s_add_u32 s54, s36, 0x20000
	v_lshl_add_u64 v[198:199], s[36:37], 0, v[132:133]
	s_addc_u32 s55, s37, 0
	s_add_i32 s53, s56, s14
	global_load_lds_dwordx4 v[198:199], off
	v_lshl_add_u64 v[208:209], s[54:55], 0, v[138:139]
	s_mov_b32 m0, s53
	v_lshl_add_u64 v[212:213], s[4:5], 0, v[134:135]
	global_load_lds_dwordx4 v[208:209], off
	v_lshl_add_u64 v[208:209], s[54:55], 0, v[132:133]
	s_add_i32 m0, s53, 0x2000
	s_nop 0
	global_load_lds_dwordx4 v[208:209], off
	v_lshl_add_u64 v[208:209], s[4:5], 0, v[140:141]
	s_mov_b32 m0, s41
	s_nop 0
	global_load_lds_dwordx4 v[208:209], off
	s_mov_b32 m0, s42
	s_nop 0
	global_load_lds_dwordx4 v[212:213], off
	s_waitcnt vmcnt(8)
	s_waitcnt lgkmcnt(0)
	s_barrier
	s_setprio 1
	s_waitcnt lgkmcnt(0)
	v_mfma_f32_16x16x32_bf16 v[64:67], v[154:157], v[186:189], v[64:67]
	v_mfma_f32_16x16x32_bf16 v[60:63], v[162:165], v[186:189], v[60:63]
	v_mfma_f32_16x16x32_bf16 v[52:55], v[154:157], v[194:197], v[52:55]
	v_mfma_f32_16x16x32_bf16 v[44:47], v[162:165], v[194:197], v[44:47]
	v_mfma_f32_16x16x32_bf16 v[36:39], v[154:157], v[228:231], v[36:39]
	v_mfma_f32_16x16x32_bf16 v[26:29], v[162:165], v[228:231], v[26:29]
	v_mfma_f32_16x16x32_bf16 v[18:21], v[154:157], v[242:245], v[18:21]
	v_mfma_f32_16x16x32_bf16 v[10:13], v[162:165], v[242:245], v[10:13]
	v_mfma_f32_16x16x32_bf16 v[64:67], v[158:161], v[190:193], v[64:67]
	v_mfma_f32_16x16x32_bf16 v[60:63], v[166:169], v[190:193], v[60:63]
	v_mfma_f32_16x16x32_bf16 v[52:55], v[158:161], v[224:227], v[52:55]
	v_mfma_f32_16x16x32_bf16 v[44:47], v[166:169], v[224:227], v[44:47]
	v_mfma_f32_16x16x32_bf16 v[36:39], v[158:161], v[238:241], v[36:39]
	v_mfma_f32_16x16x32_bf16 v[26:29], v[166:169], v[238:241], v[26:29]
	v_mfma_f32_16x16x32_bf16 v[18:21], v[158:161], v[246:249], v[18:21]
	v_mfma_f32_16x16x32_bf16 v[10:13], v[166:169], v[246:249], v[10:13]
	v_mfma_f32_16x16x32_bf16 v[56:59], v[170:173], v[186:189], v[56:59]
	v_mfma_f32_16x16x32_bf16 v[48:51], v[178:181], v[186:189], v[48:51]
	v_mfma_f32_16x16x32_bf16 v[40:43], v[170:173], v[194:197], v[40:43]
	v_mfma_f32_16x16x32_bf16 v[30:33], v[178:181], v[194:197], v[30:33]
	v_mfma_f32_16x16x32_bf16 v[22:25], v[170:173], v[228:231], v[22:25]
	v_mfma_f32_16x16x32_bf16 v[14:17], v[178:181], v[228:231], v[14:17]
	v_mfma_f32_16x16x32_bf16 v[6:9], v[170:173], v[242:245], v[6:9]
	v_mfma_f32_16x16x32_bf16 v[2:5], v[178:181], v[242:245], v[2:5]
	v_mfma_f32_16x16x32_bf16 v[56:59], v[174:177], v[190:193], v[56:59]
	v_mfma_f32_16x16x32_bf16 v[48:51], v[182:185], v[190:193], v[48:51]
	v_mfma_f32_16x16x32_bf16 v[40:43], v[174:177], v[224:227], v[40:43]
	v_mfma_f32_16x16x32_bf16 v[30:33], v[182:185], v[224:227], v[30:33]
	v_mfma_f32_16x16x32_bf16 v[22:25], v[174:177], v[238:241], v[22:25]
	v_mfma_f32_16x16x32_bf16 v[14:17], v[182:185], v[238:241], v[14:17]
	v_mfma_f32_16x16x32_bf16 v[6:9], v[174:177], v[246:249], v[6:9]
	v_mfma_f32_16x16x32_bf16 v[2:5], v[182:185], v[246:249], v[2:5]
	s_setprio 0
	s_barrier
	s_add_i32 s53, 0, 0x18000
	v_add_u32_e32 v34, s53, v1
	s_add_i32 s54, 0, 0x1c000
	ds_read_b128 v[154:157], v34
	ds_read_b128 v[158:161], v34 offset:1024
	ds_read_b128 v[162:165], v34 offset:2048
	ds_read_b128 v[166:169], v34 offset:3072
	v_add_u32_e32 v34, s54, v1
	ds_read_b128 v[170:173], v34
	ds_read_b128 v[174:177], v34 offset:1024
	ds_read_b128 v[178:181], v34 offset:2048
	ds_read_b128 v[182:185], v34 offset:3072
	s_mov_b32 m0, s43
	v_lshl_add_u64 v[232:233], s[4:5], 0, v[142:143]
	ds_read_b128 v[186:189], v152 offset:32768
	ds_read_b128 v[190:193], v152 offset:33792
	ds_read_b128 v[194:197], v152 offset:34816
	ds_read_b128 v[224:227], v152 offset:35840
	ds_read_b128 v[228:231], v152 offset:36864
	ds_read_b128 v[238:241], v152 offset:37888
	ds_read_b128 v[242:245], v152 offset:38912
	ds_read_b128 v[246:249], v152 offset:39936
	global_load_lds_dwordx4 v[232:233], off
	v_lshl_add_u64 v[232:233], s[4:5], 0, v[136:137]
	s_mov_b32 m0, s44
	s_nop 0
	global_load_lds_dwordx4 v[232:233], off
	s_waitcnt vmcnt(8)
	s_waitcnt lgkmcnt(0)
	s_barrier
	s_setprio 1
	s_waitcnt lgkmcnt(0)
	v_mfma_f32_16x16x32_bf16 v[128:131], v[154:157], v[186:189], v[128:131]
	v_mfma_f32_16x16x32_bf16 v[124:127], v[162:165], v[186:189], v[124:127]
	v_mfma_f32_16x16x32_bf16 v[116:119], v[154:157], v[194:197], v[116:119]
	v_mfma_f32_16x16x32_bf16 v[108:111], v[162:165], v[194:197], v[108:111]
	v_mfma_f32_16x16x32_bf16 v[100:103], v[154:157], v[228:231], v[100:103]
	v_mfma_f32_16x16x32_bf16 v[92:95], v[162:165], v[228:231], v[92:95]
	v_mfma_f32_16x16x32_bf16 v[84:87], v[154:157], v[242:245], v[84:87]
	v_mfma_f32_16x16x32_bf16 v[76:79], v[162:165], v[242:245], v[76:79]
	v_mfma_f32_16x16x32_bf16 v[128:131], v[158:161], v[190:193], v[128:131]
	v_mfma_f32_16x16x32_bf16 v[124:127], v[166:169], v[190:193], v[124:127]
	v_mfma_f32_16x16x32_bf16 v[116:119], v[158:161], v[224:227], v[116:119]
	v_mfma_f32_16x16x32_bf16 v[108:111], v[166:169], v[224:227], v[108:111]
	v_mfma_f32_16x16x32_bf16 v[100:103], v[158:161], v[238:241], v[100:103]
	v_mfma_f32_16x16x32_bf16 v[92:95], v[166:169], v[238:241], v[92:95]
	v_mfma_f32_16x16x32_bf16 v[84:87], v[158:161], v[246:249], v[84:87]
	v_mfma_f32_16x16x32_bf16 v[76:79], v[166:169], v[246:249], v[76:79]
	v_mfma_f32_16x16x32_bf16 v[120:123], v[170:173], v[186:189], v[120:123]
	v_mfma_f32_16x16x32_bf16 v[112:115], v[178:181], v[186:189], v[112:115]
	v_mfma_f32_16x16x32_bf16 v[104:107], v[170:173], v[194:197], v[104:107]
	v_mfma_f32_16x16x32_bf16 v[96:99], v[178:181], v[194:197], v[96:99]
	v_mfma_f32_16x16x32_bf16 v[88:91], v[170:173], v[228:231], v[88:91]
	v_mfma_f32_16x16x32_bf16 v[80:83], v[178:181], v[228:231], v[80:83]
	v_mfma_f32_16x16x32_bf16 v[72:75], v[170:173], v[242:245], v[72:75]
	v_mfma_f32_16x16x32_bf16 v[68:71], v[178:181], v[242:245], v[68:71]
	v_mfma_f32_16x16x32_bf16 v[120:123], v[174:177], v[190:193], v[120:123]
	v_mfma_f32_16x16x32_bf16 v[112:115], v[182:185], v[190:193], v[112:115]
	v_mfma_f32_16x16x32_bf16 v[104:107], v[174:177], v[224:227], v[104:107]
	v_mfma_f32_16x16x32_bf16 v[96:99], v[182:185], v[224:227], v[96:99]
	v_mfma_f32_16x16x32_bf16 v[88:91], v[174:177], v[238:241], v[88:91]
	v_mfma_f32_16x16x32_bf16 v[80:83], v[182:185], v[238:241], v[80:83]
	v_mfma_f32_16x16x32_bf16 v[72:75], v[174:177], v[246:249], v[72:75]
	v_mfma_f32_16x16x32_bf16 v[68:71], v[182:185], v[246:249], v[68:71]
	s_setprio 0
	s_barrier
	s_add_i32 s4, s53, s14
	v_lshl_add_u64 v[148:149], v[148:149], 0, s[78:79]
	s_mov_b32 m0, s4
	ds_read_b128 v[186:189], v152 offset:49152
	ds_read_b128 v[190:193], v152 offset:50176
	ds_read_b128 v[194:197], v152 offset:51200
	ds_read_b128 v[224:227], v152 offset:52224
	ds_read_b128 v[228:231], v152 offset:53248
	ds_read_b128 v[238:241], v152 offset:54272
	ds_read_b128 v[242:245], v152 offset:55296
	ds_read_b128 v[246:249], v152 offset:56320
	global_load_lds_dwordx4 v[148:149], off
	s_add_i32 m0, s4, 0x2000
	s_add_u32 s4, s36, 0x20080
	v_lshl_add_u64 v[148:149], v[198:199], 0, s[78:79]
	s_addc_u32 s5, s37, 0
	s_add_i32 s36, s54, s14
	global_load_lds_dwordx4 v[148:149], off
	v_lshl_add_u64 v[148:149], s[4:5], 0, v[138:139]
	s_mov_b32 m0, s36
	s_nop 0
	global_load_lds_dwordx4 v[148:149], off
	v_lshl_add_u64 v[148:149], s[4:5], 0, v[132:133]
	s_add_i32 m0, s36, 0x2000
	s_nop 0
	global_load_lds_dwordx4 v[148:149], off
	v_lshl_add_u64 v[148:149], v[208:209], 0, s[78:79]
	s_mov_b32 m0, s45
	s_nop 0
	global_load_lds_dwordx4 v[148:149], off
	v_lshl_add_u64 v[148:149], v[212:213], 0, s[78:79]
	s_mov_b32 m0, s46
	s_nop 0
	global_load_lds_dwordx4 v[148:149], off
	s_waitcnt vmcnt(8)
	s_waitcnt lgkmcnt(0)
	s_barrier
	s_setprio 1
	s_waitcnt lgkmcnt(0)
	v_mfma_f32_16x16x32_bf16 v[64:67], v[154:157], v[186:189], v[64:67]
	v_mfma_f32_16x16x32_bf16 v[60:63], v[162:165], v[186:189], v[60:63]
	v_mfma_f32_16x16x32_bf16 v[52:55], v[154:157], v[194:197], v[52:55]
	v_mfma_f32_16x16x32_bf16 v[44:47], v[162:165], v[194:197], v[44:47]
	v_mfma_f32_16x16x32_bf16 v[36:39], v[154:157], v[228:231], v[36:39]
	v_mfma_f32_16x16x32_bf16 v[26:29], v[162:165], v[228:231], v[26:29]
	v_mfma_f32_16x16x32_bf16 v[18:21], v[154:157], v[242:245], v[18:21]
	v_mfma_f32_16x16x32_bf16 v[10:13], v[162:165], v[242:245], v[10:13]
	v_mfma_f32_16x16x32_bf16 v[64:67], v[158:161], v[190:193], v[64:67]
	v_mfma_f32_16x16x32_bf16 v[60:63], v[166:169], v[190:193], v[60:63]
	v_mfma_f32_16x16x32_bf16 v[52:55], v[158:161], v[224:227], v[52:55]
	v_mfma_f32_16x16x32_bf16 v[44:47], v[166:169], v[224:227], v[44:47]
	v_mfma_f32_16x16x32_bf16 v[36:39], v[158:161], v[238:241], v[36:39]
	v_mfma_f32_16x16x32_bf16 v[26:29], v[166:169], v[238:241], v[26:29]
	v_mfma_f32_16x16x32_bf16 v[18:21], v[158:161], v[246:249], v[18:21]
	v_mfma_f32_16x16x32_bf16 v[10:13], v[166:169], v[246:249], v[10:13]
	v_mfma_f32_16x16x32_bf16 v[56:59], v[170:173], v[186:189], v[56:59]
	v_mfma_f32_16x16x32_bf16 v[48:51], v[178:181], v[186:189], v[48:51]
	v_mfma_f32_16x16x32_bf16 v[40:43], v[170:173], v[194:197], v[40:43]
	v_mfma_f32_16x16x32_bf16 v[30:33], v[178:181], v[194:197], v[30:33]
	v_mfma_f32_16x16x32_bf16 v[22:25], v[170:173], v[228:231], v[22:25]
	v_mfma_f32_16x16x32_bf16 v[14:17], v[178:181], v[228:231], v[14:17]
	v_mfma_f32_16x16x32_bf16 v[6:9], v[170:173], v[242:245], v[6:9]
	v_mfma_f32_16x16x32_bf16 v[2:5], v[178:181], v[242:245], v[2:5]
	v_mfma_f32_16x16x32_bf16 v[56:59], v[174:177], v[190:193], v[56:59]
	v_mfma_f32_16x16x32_bf16 v[48:51], v[182:185], v[190:193], v[48:51]
	v_mfma_f32_16x16x32_bf16 v[40:43], v[174:177], v[224:227], v[40:43]
	v_mfma_f32_16x16x32_bf16 v[30:33], v[182:185], v[224:227], v[30:33]
	v_mfma_f32_16x16x32_bf16 v[22:25], v[174:177], v[238:241], v[22:25]
	v_mfma_f32_16x16x32_bf16 v[14:17], v[182:185], v[238:241], v[14:17]
	v_mfma_f32_16x16x32_bf16 v[6:9], v[174:177], v[246:249], v[6:9]
	v_mfma_f32_16x16x32_bf16 v[2:5], v[182:185], v[246:249], v[2:5]
	s_setprio 0
	s_barrier
	s_add_i32 s52, s52, 2
	s_add_u32 s50, s50, 0x100
	s_addc_u32 s51, s51, 0
	s_add_u32 s34, s34, 0x100
	s_addc_u32 s35, s35, 0
	s_cmp_gt_u32 s52, 5
	s_cbranch_scc0 .LBB0_1199
	s_and_b64 vcc, exec, s[22:23]
	s_cbranch_vccz .LBB0_1202
	s_barrier
